# speedup vs baseline: 1.0806x; 1.0006x over previous
_Z7k_layerILi1EEvPKDF16_S1_PKfS3_S3_S3_S3_S3_S1_S1_S1_S1_S3_S3_PKhS5_PDF16_S6_PfS7_:
	s_ashr_i32 s3, s2, 1
	s_and_b32 s3, s3, -8
	s_and_b32 s16, s2, 7
	v_readfirstlane_b32 s15, v0
	s_or_b32 s12, s3, s16
	s_bfe_u32 s14, s2, 0x10003
	s_cmpk_gt_u32 s15, 0xff
	s_mov_b64 s[2:3], -1
	s_cbranch_scc0 .LBB2_17
	s_mov_b32 s44, 0x3e000000
	v_mov_b32_e32 v240, 0x64646464
	s_mov_b32 s42, 0x4010400
	s_mov_b32 s43, 0x4030402
	s_load_dwordx2 s[4:5], s[0:1], 0x80
	s_load_dwordx2 s[8:9], s[0:1], 0x0
	v_lshlrev_b32_e32 v2, 3, v0
	v_add_u32_e32 v1, 0xffffff00, v0
	v_ashrrev_i32_e32 v3, 4, v1
	v_and_b32_e32 v38, 0x78, v2
	s_lshl_b32 s17, s12, 9
	v_add_u32_e32 v2, s17, v3
	v_lshlrev_b32_e32 v4, 1, v38
	s_mov_b32 s7, 0x20000
	s_mov_b32 s6, 0x1000000
	v_lshl_or_b32 v2, v2, 8, v4
	s_waitcnt lgkmcnt(0)
	s_and_b32 s9, s9, 0xffff
	s_mov_b32 s10, s6
	s_mov_b32 s11, s7
	v_add_u32_e32 v5, 0x4000, v2
	buffer_load_dwordx4 v[10:13], v2, s[8:11], 0 offen sc1
	buffer_load_dwordx4 v[18:21], v5, s[8:11], 0 offen sc1
	v_add_u32_e32 v5, 0x1000, v2
	buffer_load_dwordx4 v[26:29], v5, s[8:11], 0 offen sc1
	v_add_u32_e32 v5, 0x2000, v2
	v_add_u32_e32 v6, 0x3000, v2
	buffer_load_dwordx4 v[30:33], v5, s[8:11], 0 offen sc1
	buffer_load_dwordx4 v[58:61], v6, s[8:11], 0 offen sc1
	v_add_u32_e32 v5, 0x5000, v2
	buffer_load_dwordx4 v[34:37], v5, s[8:11], 0 offen sc1
	v_add_u32_e32 v5, 0x6000, v2
	v_add_u32_e32 v2, 0x7000, v2
	buffer_load_dwordx4 v[62:65], v5, s[8:11], 0 offen sc1
	buffer_load_dwordx4 v[66:69], v2, s[8:11], 0 offen sc1
	s_or_b32 s2, s17, 0x80
	v_add_u32_e32 v2, s2, v3
	v_lshl_or_b32 v6, v2, 8, v4
	v_add_u32_e32 v2, 0x1000, v6
	v_add_u32_e32 v7, 0x2000, v6
	v_add_u32_e32 v8, 0x3000, v6
	buffer_load_dwordx4 v[70:73], v6, s[8:11], 0 offen sc1
	buffer_load_dwordx4 v[74:77], v2, s[8:11], 0 offen sc1
	buffer_load_dwordx4 v[14:17], v7, s[8:11], 0 offen sc1
	s_nop 0
	buffer_load_dwordx4 v[2:5], v8, s[8:11], 0 offen sc1
	v_add_u32_e32 v7, 0x4000, v6
	v_add_u32_e32 v8, 0x5000, v6
	v_add_u32_e32 v39, 0x6000, v6
	buffer_load_dwordx4 v[78:81], v7, s[8:11], 0 offen sc1
	buffer_load_dwordx4 v[82:85], v8, s[8:11], 0 offen sc1
	v_add_u32_e32 v40, 0x7000, v6
	buffer_load_dwordx4 v[22:25], v39, s[8:11], 0 offen sc1
	buffer_load_dwordx4 v[6:9], v40, s[8:11], 0 offen sc1
	v_lshlrev_b32_e32 v48, 2, v38
	v_or_b32_e32 v38, 0x1e600, v48
	s_barrier
	ds_read_b128 v[38:41], v38
	v_or_b32_e32 v42, 0x1ea00, v48
	ds_read_b128 v[42:45], v42
	v_or_b32_e32 v49, 0x1e800, v48
	v_or_b32_e32 v50, 0x1ec00, v48
	s_waitcnt lgkmcnt(1)
	v_cvt_pk_f16_f32 v46, v38, v39
	v_or_b32_e32 v38, 0x1e610, v48
	v_cvt_pk_f16_f32 v47, v40, v41
	ds_read_b128 v[38:41], v38
	v_or_b32_e32 v51, 0x1ea10, v48
	ds_read_b128 v[54:57], v49
	ds_read_b128 v[86:89], v50
	ds_read_b128 v[90:93], v51
	v_or_b32_e32 v94, 0x1e810, v48
	v_or_b32_e32 v48, 0x1ec10, v48
	s_waitcnt lgkmcnt(3)
	v_cvt_pk_f16_f32 v51, v38, v39
	s_waitcnt lgkmcnt(2)
	v_pk_fma_f32 v[38:39], v[54:55], 0, v[42:43] op_sel_hi:[1,0,1]
	v_cvt_pk_f16_f32 v52, v40, v41
	s_waitcnt lgkmcnt(1)
	v_pk_add_f32 v[38:39], v[86:87], v[38:39]
	v_pk_fma_f32 v[42:43], v[56:57], 0, v[44:45] op_sel_hi:[1,0,1]
	v_cvt_pk_f16_f32 v53, v38, v39
	ds_read_b128 v[38:41], v94
	ds_read_b128 v[94:97], v48
	v_pk_add_f32 v[42:43], v[88:89], v[42:43]
	s_movk_i32 s13, 0x110
	v_cvt_pk_f16_f32 v55, v42, v43
	s_waitcnt lgkmcnt(1)
	v_pk_fma_f32 v[38:39], v[38:39], 0, v[90:91] op_sel_hi:[1,0,1]
	s_or_b32 s20, s17, 0x100
	s_waitcnt lgkmcnt(0)
	v_pk_add_f32 v[38:39], v[94:95], v[38:39]
	s_or_b32 s18, s17, 0x180
	v_cvt_pk_f16_f32 v56, v38, v39
	v_pk_fma_f32 v[38:39], v[40:41], 0, v[92:93] op_sel_hi:[1,0,1]
	s_lshl_b32 s17, s14, 6
	v_pk_add_f32 v[38:39], v[96:97], v[38:39]
	v_mov_b32_e32 v122, 0x11000
	v_cvt_pk_f16_f32 v57, v38, v39
	v_mov_b32_e32 v38, v0
	s_and_b32 s5, s5, 0xffff
	v_add_u32_e32 v39, 0xffffff00, v38
	v_lshlrev_b32_e32 v38, 4, v38
	v_ashrrev_i32_e32 v39, 4, v39
	v_and_b32_e32 v40, 0xf0, v38
	v_mad_u64_u32 v[42:43], s[22:23], v39, s13, v[40:41]
	s_lshl_b32 s2, s2, 7
	s_or_b32 s2, s2, s17
	s_mov_b32 s3, 0
	s_lshr_b32 s19, s15, 6
	s_movk_i32 s21, 0x1000
	s_waitcnt vmcnt(15)
	v_pk_fma_f16 v12, v51, v12, v56
	v_pk_fma_f16 v10, v46, v10, v53
	v_pk_fma_f16 v13, v52, v13, v57
	v_pk_fma_f16 v11, v47, v11, v55
	s_waitcnt vmcnt(14)
	v_pk_fma_f16 v20, v51, v20, v56
	v_pk_fma_f16 v18, v46, v18, v53
	v_pk_fma_f16 v21, v52, v21, v57
	v_pk_fma_f16 v19, v47, v19, v55
	ds_write_b128 v42, v[10:13]
	ds_write_b128 v42, v[18:21] offset:17408
	v_pk_add_f16 v44, v13, v21
	v_pk_add_f16 v48, v12, v20
	v_pk_add_f16 v54, v11, v19
	v_pk_add_f16 v114, v10, v18
	s_waitcnt vmcnt(13)
	v_pk_fma_f16 v12, v51, v28, v56
	v_pk_fma_f16 v10, v46, v26, v53
	v_pk_fma_f16 v13, v52, v29, v57
	v_pk_fma_f16 v11, v47, v27, v55
	s_waitcnt vmcnt(10)
	v_pk_fma_f16 v20, v51, v36, v56
	v_pk_fma_f16 v18, v46, v34, v53
	v_pk_fma_f16 v21, v52, v37, v57
	v_pk_fma_f16 v19, v47, v35, v55
	ds_write_b128 v42, v[10:13] offset:4352
	ds_write_b128 v42, v[18:21] offset:21760
	v_pk_add_f16 v36, v13, v21
	v_pk_add_f16 v38, v12, v20
	v_pk_add_f16 v41, v11, v19
	v_pk_add_f16 v43, v10, v18
	v_pk_fma_f16 v12, v51, v32, v56
	v_pk_fma_f16 v10, v46, v30, v53
	v_pk_fma_f16 v13, v52, v33, v57
	v_pk_fma_f16 v11, v47, v31, v55
	s_waitcnt vmcnt(9)
	v_pk_fma_f16 v20, v51, v64, v56
	v_pk_fma_f16 v18, v46, v62, v53
	v_pk_fma_f16 v21, v52, v65, v57
	v_pk_fma_f16 v19, v47, v63, v55
	ds_write_b128 v42, v[10:13] offset:8704
	ds_write_b128 v42, v[18:21] offset:26112
	v_pk_add_f16 v30, v13, v21
	v_pk_add_f16 v31, v12, v20
	v_pk_add_f16 v33, v11, v19
	v_pk_add_f16 v35, v10, v18
	v_pk_fma_f16 v12, v51, v60, v56
	v_pk_fma_f16 v10, v46, v58, v53
	v_pk_fma_f16 v13, v52, v61, v57
	v_pk_fma_f16 v11, v47, v59, v55
	s_waitcnt vmcnt(8)
	v_pk_fma_f16 v18, v46, v66, v53
	v_pk_fma_f16 v20, v51, v68, v56
	v_pk_fma_f16 v21, v52, v69, v57
	v_pk_fma_f16 v19, v47, v67, v55
	ds_write_b128 v42, v[10:13] offset:13056
	ds_write_b128 v42, v[18:21] offset:30464
	s_waitcnt lgkmcnt(0)
	s_barrier
	v_pk_add_f16 v29, v10, v18
	v_add_u32_e32 v10, s20, v39
	v_lshl_or_b32 v18, v10, 8, v40
	v_pk_add_f16 v28, v11, v19
	v_add_u32_e32 v10, 0x1000, v18
	v_add_u32_e32 v19, 0x2000, v18
	v_pk_add_f16 v26, v13, v21
	v_pk_add_f16 v27, v12, v20
	buffer_load_dwordx4 v[60:63], v18, s[8:11], 0 offen sc1
	buffer_load_dwordx4 v[64:67], v10, s[8:11], 0 offen sc1
	v_add_u32_e32 v20, 0x3000, v18
	buffer_load_dwordx4 v[86:89], v19, s[8:11], 0 offen sc1
	buffer_load_dwordx4 v[10:13], v20, s[8:11], 0 offen sc1
	v_add_u32_e32 v19, 0x4000, v18
	v_add_u32_e32 v20, 0x5000, v18
	buffer_load_dwordx4 v[90:93], v19, s[8:11], 0 offen sc1
	buffer_load_dwordx4 v[94:97], v20, s[8:11], 0 offen sc1
	v_add_u32_e32 v32, 0x6000, v18
	v_add_u32_e32 v34, 0x7000, v18
	buffer_load_dwordx4 v[98:101], v32, s[8:11], 0 offen sc1
	buffer_load_dwordx4 v[18:21], v34, s[8:11], 0 offen sc1
	v_mov_b32_e32 v32, v0
	s_waitcnt vmcnt(15)
	v_pk_fma_f16 v72, v51, v72, v56
	v_add_u32_e32 v34, 0xffffff00, v32
	v_lshlrev_b32_e32 v32, 4, v32
	v_ashrrev_i32_e32 v59, 4, v34
	v_and_b32_e32 v102, 0xf0, v32
	v_pk_fma_f16 v70, v46, v70, v53
	v_pk_fma_f16 v73, v52, v73, v57
	v_pk_fma_f16 v71, v47, v71, v55
	s_waitcnt vmcnt(11)
	v_pk_fma_f16 v78, v46, v78, v53
	v_pk_fma_f16 v79, v47, v79, v55
	v_mad_u64_u32 v[104:105], s[22:23], v59, s13, v[102:103]
	v_pk_fma_f16 v80, v51, v80, v56
	v_pk_fma_f16 v81, v52, v81, v57
	ds_write_b128 v104, v[70:73] offset:34816
	ds_write_b128 v104, v[78:81] offset:52224
	v_pk_add_f16 v117, v71, v79
	v_pk_add_f16 v118, v70, v78
	v_pk_fma_f16 v70, v51, v76, v56
	v_pk_fma_f16 v68, v46, v74, v53
	v_pk_fma_f16 v71, v52, v77, v57
	v_pk_fma_f16 v69, v47, v75, v55
	v_pk_fma_f16 v16, v51, v16, v56
	v_pk_fma_f16 v14, v46, v14, v53
	v_pk_fma_f16 v17, v52, v17, v57
	v_pk_fma_f16 v15, v47, v15, v55
	v_pk_fma_f16 v4, v51, v4, v56
	v_pk_fma_f16 v2, v46, v2, v53
	v_pk_fma_f16 v5, v52, v5, v57
	v_pk_fma_f16 v3, v47, v3, v55
	s_waitcnt vmcnt(8)
	v_pk_fma_f16 v6, v46, v6, v53
	v_pk_add_f16 v115, v73, v81
	v_pk_add_f16 v116, v72, v80
	v_pk_fma_f16 v74, v51, v84, v56
	v_pk_fma_f16 v72, v46, v82, v53
	v_pk_fma_f16 v75, v52, v85, v57
	v_pk_fma_f16 v73, v47, v83, v55
	ds_write_b128 v104, v[68:71] offset:39168
	ds_write_b128 v104, v[72:75] offset:56576
	v_pk_fma_f16 v24, v51, v24, v56
	v_pk_fma_f16 v22, v46, v22, v53
	v_pk_fma_f16 v25, v52, v25, v57
	v_pk_fma_f16 v23, v47, v23, v55
	ds_write_b128 v104, v[14:17] offset:43520
	ds_write_b128 v104, v[22:25] offset:60928
	v_pk_fma_f16 v8, v51, v8, v56
	v_pk_fma_f16 v9, v52, v9, v57
	v_pk_fma_f16 v7, v47, v7, v55
	ds_write_b128 v104, v[2:5] offset:47872
	ds_write_b128 v104, v[6:9] offset:65280
	v_pk_add_f16 v39, v2, v6
	v_add_u32_e32 v2, s18, v59
	v_lshl_or_b32 v6, v2, 8, v102
	v_pk_add_f16 v34, v4, v8
	v_pk_add_f16 v37, v3, v7
	v_add_u32_e32 v2, 0x1000, v6
	v_add_u32_e32 v7, 0x2000, v6
	v_add_u32_e32 v8, 0x3000, v6
	v_pk_add_f16 v50, v71, v75
	v_pk_add_f16 v58, v70, v74
	v_pk_add_f16 v119, v69, v73
	v_pk_add_f16 v120, v68, v72
	v_pk_add_f16 v40, v17, v25
	v_pk_add_f16 v42, v16, v24
	v_pk_add_f16 v45, v15, v23
	v_pk_add_f16 v49, v14, v22
	v_pk_add_f16 v32, v5, v9
	buffer_load_dwordx4 v[68:71], v6, s[8:11], 0 offen sc1
	buffer_load_dwordx4 v[72:75], v2, s[8:11], 0 offen sc1
	buffer_load_dwordx4 v[14:17], v7, s[8:11], 0 offen sc1
	s_nop 0
	buffer_load_dwordx4 v[2:5], v8, s[8:11], 0 offen sc1
	v_add_u32_e32 v7, 0x4000, v6
	v_add_u32_e32 v8, 0x5000, v6
	v_add_u32_e32 v59, 0x6000, v6
	buffer_load_dwordx4 v[76:79], v7, s[8:11], 0 offen sc1
	buffer_load_dwordx4 v[80:83], v8, s[8:11], 0 offen sc1
	v_add_u32_e32 v84, 0x7000, v6
	buffer_load_dwordx4 v[22:25], v59, s[8:11], 0 offen sc1
	buffer_load_dwordx4 v[6:9], v84, s[8:11], 0 offen sc1
	v_mov_b32_e32 v59, v0
	v_fma_mix_f32 v192, v114, s44, 0 op_sel_hi:[1,0,0]
	v_fma_mix_f32 v193, v114, s44, 0 op_sel:[1,0,0] op_sel_hi:[1,0,0]
	v_fma_mix_f32 v192, v118, s44, v192 op_sel_hi:[1,0,0]
	v_fma_mix_f32 v193, v118, s44, v193 op_sel:[1,0,0] op_sel_hi:[1,0,0]
	v_fma_mix_f32 v194, v54, s44, 0 op_sel_hi:[1,0,0]
	v_fma_mix_f32 v195, v54, s44, 0 op_sel:[1,0,0] op_sel_hi:[1,0,0]
	v_fma_mix_f32 v194, v117, s44, v194 op_sel_hi:[1,0,0]
	v_fma_mix_f32 v195, v117, s44, v195 op_sel:[1,0,0] op_sel_hi:[1,0,0]
	v_fma_mix_f32 v196, v48, s44, 0 op_sel_hi:[1,0,0]
	v_fma_mix_f32 v197, v48, s44, 0 op_sel:[1,0,0] op_sel_hi:[1,0,0]
	v_fma_mix_f32 v196, v116, s44, v196 op_sel_hi:[1,0,0]
	v_fma_mix_f32 v197, v116, s44, v197 op_sel:[1,0,0] op_sel_hi:[1,0,0]
	v_fma_mix_f32 v198, v44, s44, 0 op_sel_hi:[1,0,0]
	v_fma_mix_f32 v199, v44, s44, 0 op_sel:[1,0,0] op_sel_hi:[1,0,0]
	v_fma_mix_f32 v198, v115, s44, v198 op_sel_hi:[1,0,0]
	v_fma_mix_f32 v199, v115, s44, v199 op_sel:[1,0,0] op_sel_hi:[1,0,0]
	v_fma_mix_f32 v200, v43, s44, 0 op_sel_hi:[1,0,0]
	v_fma_mix_f32 v201, v43, s44, 0 op_sel:[1,0,0] op_sel_hi:[1,0,0]
	v_fma_mix_f32 v200, v120, s44, v200 op_sel_hi:[1,0,0]
	v_fma_mix_f32 v201, v120, s44, v201 op_sel:[1,0,0] op_sel_hi:[1,0,0]
	v_fma_mix_f32 v202, v41, s44, 0 op_sel_hi:[1,0,0]
	v_fma_mix_f32 v203, v41, s44, 0 op_sel:[1,0,0] op_sel_hi:[1,0,0]
	v_fma_mix_f32 v202, v119, s44, v202 op_sel_hi:[1,0,0]
	v_fma_mix_f32 v203, v119, s44, v203 op_sel:[1,0,0] op_sel_hi:[1,0,0]
	v_fma_mix_f32 v204, v38, s44, 0 op_sel_hi:[1,0,0]
	v_fma_mix_f32 v205, v38, s44, 0 op_sel:[1,0,0] op_sel_hi:[1,0,0]
	v_fma_mix_f32 v204, v58, s44, v204 op_sel_hi:[1,0,0]
	v_fma_mix_f32 v205, v58, s44, v205 op_sel:[1,0,0] op_sel_hi:[1,0,0]
	v_fma_mix_f32 v206, v36, s44, 0 op_sel_hi:[1,0,0]
	v_fma_mix_f32 v207, v36, s44, 0 op_sel:[1,0,0] op_sel_hi:[1,0,0]
	v_fma_mix_f32 v206, v50, s44, v206 op_sel_hi:[1,0,0]
	v_fma_mix_f32 v207, v50, s44, v207 op_sel:[1,0,0] op_sel_hi:[1,0,0]
	v_fma_mix_f32 v208, v35, s44, 0 op_sel_hi:[1,0,0]
	v_fma_mix_f32 v209, v35, s44, 0 op_sel:[1,0,0] op_sel_hi:[1,0,0]
	v_fma_mix_f32 v208, v49, s44, v208 op_sel_hi:[1,0,0]
	v_fma_mix_f32 v209, v49, s44, v209 op_sel:[1,0,0] op_sel_hi:[1,0,0]
	v_fma_mix_f32 v210, v33, s44, 0 op_sel_hi:[1,0,0]
	v_fma_mix_f32 v211, v33, s44, 0 op_sel:[1,0,0] op_sel_hi:[1,0,0]
	v_fma_mix_f32 v210, v45, s44, v210 op_sel_hi:[1,0,0]
	v_fma_mix_f32 v211, v45, s44, v211 op_sel:[1,0,0] op_sel_hi:[1,0,0]
	v_fma_mix_f32 v212, v31, s44, 0 op_sel_hi:[1,0,0]
	v_fma_mix_f32 v213, v31, s44, 0 op_sel:[1,0,0] op_sel_hi:[1,0,0]
	v_fma_mix_f32 v212, v42, s44, v212 op_sel_hi:[1,0,0]
	v_fma_mix_f32 v213, v42, s44, v213 op_sel:[1,0,0] op_sel_hi:[1,0,0]
	v_fma_mix_f32 v214, v30, s44, 0 op_sel_hi:[1,0,0]
	v_fma_mix_f32 v215, v30, s44, 0 op_sel:[1,0,0] op_sel_hi:[1,0,0]
	v_fma_mix_f32 v214, v40, s44, v214 op_sel_hi:[1,0,0]
	v_fma_mix_f32 v215, v40, s44, v215 op_sel:[1,0,0] op_sel_hi:[1,0,0]
	v_fma_mix_f32 v216, v29, s44, 0 op_sel_hi:[1,0,0]
	v_fma_mix_f32 v217, v29, s44, 0 op_sel:[1,0,0] op_sel_hi:[1,0,0]
	v_fma_mix_f32 v216, v39, s44, v216 op_sel_hi:[1,0,0]
	v_fma_mix_f32 v217, v39, s44, v217 op_sel:[1,0,0] op_sel_hi:[1,0,0]
	v_fma_mix_f32 v218, v28, s44, 0 op_sel_hi:[1,0,0]
	v_fma_mix_f32 v219, v28, s44, 0 op_sel:[1,0,0] op_sel_hi:[1,0,0]
	v_fma_mix_f32 v218, v37, s44, v218 op_sel_hi:[1,0,0]
	v_fma_mix_f32 v219, v37, s44, v219 op_sel:[1,0,0] op_sel_hi:[1,0,0]
	v_fma_mix_f32 v220, v27, s44, 0 op_sel_hi:[1,0,0]
	v_fma_mix_f32 v221, v27, s44, 0 op_sel:[1,0,0] op_sel_hi:[1,0,0]
	v_fma_mix_f32 v220, v34, s44, v220 op_sel_hi:[1,0,0]
	v_fma_mix_f32 v221, v34, s44, v221 op_sel:[1,0,0] op_sel_hi:[1,0,0]
	v_fma_mix_f32 v222, v26, s44, 0 op_sel_hi:[1,0,0]
	v_fma_mix_f32 v223, v26, s44, 0 op_sel:[1,0,0] op_sel_hi:[1,0,0]
	v_fma_mix_f32 v222, v32, s44, v222 op_sel_hi:[1,0,0]
	v_fma_mix_f32 v223, v32, s44, v223 op_sel:[1,0,0] op_sel_hi:[1,0,0]
	s_waitcnt lgkmcnt(0)
	s_barrier
	s_lshl_b32 s8, s12, 16
	v_add_u32_e32 v85, 0xffffff00, v59
	v_lshlrev_b32_e32 v84, 3, v59
	v_lshrrev_b32_e32 v121, 4, v85
	v_and_b32_e32 v102, 56, v84
	v_lshrrev_b32_e32 v110, 3, v85
	v_ashrrev_i32_e32 v85, 3, v85
	s_movk_i32 s10, 0xffc0
	s_or_b32 s8, s8, s17
	v_lshl_or_b32 v84, v102, 1, v122
	v_bfi_b32 v85, s10, v85, v110
	s_movk_i32 s11, 0x90
	v_or_b32_e32 v106, s8, v102
	v_mad_u64_u32 v[102:103], s[8:9], v85, s11, v[84:85]
	ds_read_b128 v[102:105], v102
	v_lshlrev_b32_e32 v123, 1, v106
	v_lshrrev_b32_e32 v111, 3, v59
	v_ashrrev_i32_e32 v106, 3, v59
	v_lshl_add_u32 v85, v85, 8, v123
	v_bfi_b32 v112, s10, v106, v111
	v_mad_u64_u32 v[106:107], s[8:9], v112, s11, v[84:85]
	ds_read_b128 v[106:109], v106
	s_waitcnt lgkmcnt(1)
	buffer_store_dwordx4 v[102:105], v85, s[4:7], 0 offen sc1
	v_add_u32_e32 v85, 0x100, v59
	v_ashrrev_i32_e32 v85, 3, v85
	v_bfi_b32 v125, s10, v85, v110
	v_mad_u64_u32 v[102:103], s[8:9], v125, s11, v[84:85]
	v_add_u32_e32 v85, 0x200, v59
	v_ashrrev_i32_e32 v85, 3, v85
	v_bfi_b32 v126, s10, v85, v111
	ds_read_b128 v[102:105], v102
	v_mad_u64_u32 v[84:85], s[8:9], v126, s11, v[84:85]
	v_lshl_add_u32 v124, v112, 8, v123
	ds_read_b128 v[110:113], v84
	v_lshl_add_u32 v84, v125, 8, v123
	s_waitcnt lgkmcnt(2)
	buffer_store_dwordx4 v[106:109], v124, s[4:7], 0 offen sc1
	s_waitcnt lgkmcnt(1)
	buffer_store_dwordx4 v[102:105], v84, s[4:7], 0 offen sc1
	v_lshl_add_u32 v84, v126, 8, v123
	v_lshlrev_b32_e32 v59, 4, v59
	s_waitcnt lgkmcnt(0)
	buffer_store_dwordx4 v[110:113], v84, s[4:7], 0 offen sc1
	v_and_b32_e32 v84, 0xf0, v59
	s_waitcnt vmcnt(19)
	v_pk_fma_f16 v63, v52, v63, v57
	v_pk_fma_f16 v62, v51, v62, v56
	v_pk_fma_f16 v61, v47, v61, v55
	v_pk_fma_f16 v60, v46, v60, v53
	s_waitcnt vmcnt(15)
	v_pk_fma_f16 v93, v52, v93, v57
	v_pk_fma_f16 v92, v51, v92, v56
	v_pk_fma_f16 v91, v47, v91, v55
	v_pk_fma_f16 v90, v46, v90, v53
	v_mad_u64_u32 v[84:85], s[8:9], v121, s13, v[84:85]
	ds_write_b128 v84, v[60:63]
	ds_write_b128 v84, v[90:93] offset:17408
	v_pk_add_f16 v59, v63, v93
	v_pk_add_f16 v85, v62, v92
	v_pk_add_f16 v91, v61, v91
	v_pk_add_f16 v90, v60, v90
	v_pk_fma_f16 v63, v52, v67, v57
	v_pk_fma_f16 v62, v51, v66, v56
	v_pk_fma_f16 v61, v47, v65, v55
	v_pk_fma_f16 v60, v46, v64, v53
	s_waitcnt vmcnt(14)
	v_pk_fma_f16 v67, v52, v97, v57
	v_pk_fma_f16 v66, v51, v96, v56
	v_pk_fma_f16 v65, v47, v95, v55
	v_pk_fma_f16 v64, v46, v94, v53
	ds_write_b128 v84, v[60:63] offset:4352
	ds_write_b128 v84, v[64:67] offset:21760
	v_pk_add_f16 v92, v63, v67
	v_pk_add_f16 v93, v62, v66
	v_pk_add_f16 v94, v61, v65
	v_pk_add_f16 v95, v60, v64
	v_pk_fma_f16 v63, v52, v89, v57
	v_pk_fma_f16 v62, v51, v88, v56
	v_pk_fma_f16 v61, v47, v87, v55
	v_pk_fma_f16 v60, v46, v86, v53
	s_waitcnt vmcnt(13)
	v_pk_fma_f16 v67, v52, v101, v57
	v_pk_fma_f16 v66, v51, v100, v56
	v_pk_fma_f16 v65, v47, v99, v55
	v_pk_fma_f16 v64, v46, v98, v53
	ds_write_b128 v84, v[60:63] offset:8704
	ds_write_b128 v84, v[64:67] offset:26112
	v_pk_add_f16 v86, v63, v67
	v_pk_add_f16 v87, v62, v66
	v_pk_add_f16 v88, v61, v65
	v_pk_add_f16 v89, v60, v64
	v_pk_fma_f16 v63, v52, v13, v57
	v_pk_fma_f16 v62, v51, v12, v56
	v_pk_fma_f16 v61, v47, v11, v55
	v_pk_fma_f16 v60, v46, v10, v53
	v_mov_b32_e32 v97, v0
	s_waitcnt vmcnt(12)
	v_pk_fma_f16 v21, v52, v21, v57
	v_pk_fma_f16 v20, v51, v20, v56
	v_pk_fma_f16 v19, v47, v19, v55
	v_pk_fma_f16 v18, v46, v18, v53
	ds_write_b128 v84, v[60:63] offset:13056
	ds_write_b128 v84, v[18:21] offset:30464
	s_waitcnt lgkmcnt(0)
	s_barrier
	v_pk_add_f16 v96, v60, v18
	v_add_u32_e32 v13, 0xffffff00, v97
	v_lshlrev_b32_e32 v12, 3, v97
	v_lshrrev_b32_e32 v98, 4, v13
	v_and_b32_e32 v18, 56, v12
	v_lshrrev_b32_e32 v64, 3, v13
	v_ashrrev_i32_e32 v13, 3, v13
	v_lshl_or_b32 v12, v18, 1, v122
	v_bfi_b32 v13, s10, v13, v64
	v_pk_add_f16 v84, v61, v19
	v_or_b32_e32 v60, s2, v18
	v_mad_u64_u32 v[18:19], s[8:9], v13, s11, v[12:13]
	v_pk_add_f16 v10, v63, v21
	v_pk_add_f16 v11, v62, v20
	ds_read_b128 v[18:21], v18 offset:18432
	v_lshlrev_b32_e32 v99, 1, v60
	v_lshrrev_b32_e32 v65, 3, v97
	v_ashrrev_i32_e32 v60, 3, v97
	v_lshl_add_u32 v13, v13, 8, v99
	v_bfi_b32 v66, s10, v60, v65
	v_mad_u64_u32 v[60:61], s[8:9], v66, s11, v[12:13]
	ds_read_b128 v[60:63], v60 offset:18432
	s_waitcnt lgkmcnt(1)
	buffer_store_dwordx4 v[18:21], v13, s[4:7], 0 offen sc1
	v_add_u32_e32 v13, 0x100, v97
	v_ashrrev_i32_e32 v13, 3, v13
	v_bfi_b32 v101, s10, v13, v64
	v_mad_u64_u32 v[18:19], s[8:9], v101, s11, v[12:13]
	v_add_u32_e32 v13, 0x200, v97
	v_ashrrev_i32_e32 v13, 3, v13
	v_bfi_b32 v102, s10, v13, v65
	ds_read_b128 v[18:21], v18 offset:18432
	v_mad_u64_u32 v[12:13], s[8:9], v102, s11, v[12:13]
	v_lshl_add_u32 v100, v66, 8, v99
	ds_read_b128 v[64:67], v12 offset:18432
	v_lshl_add_u32 v12, v101, 8, v99
	s_waitcnt lgkmcnt(2)
	buffer_store_dwordx4 v[60:63], v100, s[4:7], 0 offen sc1
	s_waitcnt lgkmcnt(1)
	buffer_store_dwordx4 v[18:21], v12, s[4:7], 0 offen sc1
	v_lshl_add_u32 v12, v102, 8, v99
	s_waitcnt lgkmcnt(0)
	buffer_store_dwordx4 v[64:67], v12, s[4:7], 0 offen sc1
	v_lshlrev_b32_e32 v12, 4, v97
	v_and_b32_e32 v12, 0xf0, v12
	s_waitcnt vmcnt(15)
	v_pk_fma_f16 v21, v52, v71, v57
	v_pk_fma_f16 v20, v51, v70, v56
	v_pk_fma_f16 v19, v47, v69, v55
	v_pk_fma_f16 v18, v46, v68, v53
	s_waitcnt vmcnt(11)
	v_pk_fma_f16 v63, v52, v79, v57
	v_pk_fma_f16 v62, v51, v78, v56
	v_pk_fma_f16 v61, v47, v77, v55
	v_pk_fma_f16 v60, v46, v76, v53
	v_mad_u64_u32 v[12:13], s[8:9], v98, s13, v[12:13]
	ds_write_b128 v12, v[18:21] offset:34816
	ds_write_b128 v12, v[60:63] offset:52224
	v_pk_add_f16 v13, v21, v63
	v_pk_add_f16 v64, v20, v62
	v_pk_add_f16 v65, v19, v61
	v_pk_add_f16 v66, v18, v60
	v_pk_fma_f16 v21, v52, v75, v57
	v_pk_fma_f16 v20, v51, v74, v56
	v_pk_fma_f16 v19, v47, v73, v55
	v_pk_fma_f16 v18, v46, v72, v53
	s_waitcnt vmcnt(10)
	v_pk_fma_f16 v63, v52, v83, v57
	v_pk_fma_f16 v62, v51, v82, v56
	v_pk_fma_f16 v61, v47, v81, v55
	v_pk_fma_f16 v60, v46, v80, v53
	v_pk_fma_f16 v17, v52, v17, v57
	v_pk_fma_f16 v16, v51, v16, v56
	v_pk_fma_f16 v15, v47, v15, v55
	v_pk_fma_f16 v14, v46, v14, v53
	v_pk_fma_f16 v5, v52, v5, v57
	v_pk_fma_f16 v4, v51, v4, v56
	v_pk_fma_f16 v3, v47, v3, v55
	v_pk_fma_f16 v2, v46, v2, v53
	s_waitcnt vmcnt(8)
	v_pk_fma_f16 v7, v47, v7, v55
	v_pk_fma_f16 v6, v46, v6, v53
	ds_write_b128 v12, v[18:21] offset:39168
	ds_write_b128 v12, v[60:63] offset:56576
	v_pk_add_f16 v63, v21, v63
	v_pk_add_f16 v62, v20, v62
	v_pk_add_f16 v61, v19, v61
	v_pk_add_f16 v60, v18, v60
	v_pk_fma_f16 v21, v52, v25, v57
	v_pk_fma_f16 v20, v51, v24, v56
	v_pk_fma_f16 v19, v47, v23, v55
	v_pk_fma_f16 v18, v46, v22, v53
	ds_write_b128 v12, v[14:17] offset:43520
	ds_write_b128 v12, v[18:21] offset:60928
	v_pk_fma_f16 v9, v52, v9, v57
	v_pk_fma_f16 v8, v51, v8, v56
	ds_write_b128 v12, v[2:5] offset:47872
	ds_write_b128 v12, v[6:9] offset:65280
	v_pk_add_f16 v24, v3, v7
	v_pk_add_f16 v25, v2, v6
	v_pk_add_f16 v22, v5, v9
	v_pk_add_f16 v23, v4, v8
	v_fma_mix_f32 v192, v90, s44, v192 op_sel_hi:[1,0,0]
	v_fma_mix_f32 v193, v90, s44, v193 op_sel:[1,0,0] op_sel_hi:[1,0,0]
	v_fma_mixlo_f16 v224, v66, s44, v192 op_sel_hi:[1,0,0]
	s_nop 0
	v_fma_mixhi_f16 v224, v66, s44, v193 op_sel:[1,0,0] op_sel_hi:[1,0,0]
	v_pk_add_f16 v19, v15, v19
	v_fma_mix_f32 v194, v91, s44, v194 op_sel_hi:[1,0,0]
	v_fma_mix_f32 v195, v91, s44, v195 op_sel:[1,0,0] op_sel_hi:[1,0,0]
	v_pk_add_f16 v18, v14, v18
	v_fma_mixlo_f16 v225, v65, s44, v194 op_sel_hi:[1,0,0]
	s_nop 0
	v_fma_mixhi_f16 v225, v65, s44, v195 op_sel:[1,0,0] op_sel_hi:[1,0,0]
	s_mov_b32 s2, 0x3e000000
	v_fma_mix_f32 v196, v85, s44, v196 op_sel_hi:[1,0,0]
	v_fma_mix_f32 v197, v85, s44, v197 op_sel:[1,0,0] op_sel_hi:[1,0,0]
	v_fma_mixlo_f16 v226, v64, s44, v196 op_sel_hi:[1,0,0]
	s_nop 0
	v_fma_mixhi_f16 v226, v64, s44, v197 op_sel:[1,0,0] op_sel_hi:[1,0,0]
	v_pk_add_f16 v21, v17, v21
	v_fma_mix_f32 v198, v59, s44, v198 op_sel_hi:[1,0,0]
	v_fma_mix_f32 v199, v59, s44, v199 op_sel:[1,0,0] op_sel_hi:[1,0,0]
	v_pk_add_f16 v20, v16, v20
	v_fma_mixlo_f16 v227, v13, s44, v198 op_sel_hi:[1,0,0]
	s_nop 0
	v_fma_mixhi_f16 v227, v13, s44, v199 op_sel:[1,0,0] op_sel_hi:[1,0,0]
	v_fma_mix_f32 v200, v60, s44, v200 op_sel_hi:[1,0,0]
	v_add_u32_e32 v16, 0x1a000, v12
	v_fma_mix_f32 v201, v60, s44, v201 op_sel:[1,0,0] op_sel_hi:[1,0,0]
	ds_write_b128 v16, v[224:227]
	v_fma_mixlo_f16 v228, v95, s44, v200 op_sel_hi:[1,0,0]
	s_nop 0
	v_fma_mixhi_f16 v228, v95, s44, v201 op_sel:[1,0,0] op_sel_hi:[1,0,0]
	v_fma_mix_f32 v202, v61, s44, v202 op_sel_hi:[1,0,0]
	s_nop 0
	v_fma_mixlo_f16 v229, v94, s44, v202 op_sel_hi:[1,0,0]
	v_fma_mix_f32 v203, v94, s44, v203 op_sel:[1,0,0] op_sel_hi:[1,0,0]
	v_fma_mixhi_f16 v229, v61, s44, v203 op_sel:[1,0,0] op_sel_hi:[1,0,0]
	v_fma_mix_f32 v204, v93, s44, v204 op_sel_hi:[1,0,0]
	v_fma_mix_f32 v205, v93, s44, v205 op_sel:[1,0,0] op_sel_hi:[1,0,0]
	v_fma_mixlo_f16 v230, v62, s44, v204 op_sel_hi:[1,0,0]
	s_nop 0
	v_fma_mixhi_f16 v230, v62, s44, v205 op_sel:[1,0,0] op_sel_hi:[1,0,0]
	v_fma_mix_f32 v206, v63, s44, v206 op_sel_hi:[1,0,0]
	s_nop 0
	v_fma_mixlo_f16 v231, v92, s44, v206 op_sel_hi:[1,0,0]
	v_fma_mix_f32 v207, v92, s44, v207 op_sel:[1,0,0] op_sel_hi:[1,0,0]
	v_fma_mixhi_f16 v231, v63, s44, v207 op_sel:[1,0,0] op_sel_hi:[1,0,0]
	v_fma_mix_f32 v208, v18, s44, v208 op_sel_hi:[1,0,0]
	v_fma_mix_f32 v209, v18, s44, v209 op_sel:[1,0,0] op_sel_hi:[1,0,0]
	v_fma_mix_f32 v210, v19, s44, v210 op_sel_hi:[1,0,0]
	ds_write_b128 v16, v[228:231] offset:4352
	v_fma_mixlo_f16 v232, v89, s44, v208 op_sel_hi:[1,0,0]
	s_nop 0
	v_fma_mixhi_f16 v232, v89, s44, v209 op_sel:[1,0,0] op_sel_hi:[1,0,0]
	v_fma_mix_f32 v211, v19, s44, v211 op_sel:[1,0,0] op_sel_hi:[1,0,0]
	v_fma_mixlo_f16 v233, v88, s44, v210 op_sel_hi:[1,0,0]
	s_nop 0
	v_fma_mixhi_f16 v233, v88, s44, v211 op_sel:[1,0,0] op_sel_hi:[1,0,0]
	v_fma_mix_f32 v212, v87, s44, v212 op_sel_hi:[1,0,0]
	v_fma_mix_f32 v213, v87, s44, v213 op_sel:[1,0,0] op_sel_hi:[1,0,0]
	v_fma_mixlo_f16 v234, v20, s44, v212 op_sel_hi:[1,0,0]
	s_nop 0
	v_fma_mixhi_f16 v234, v20, s44, v213 op_sel:[1,0,0] op_sel_hi:[1,0,0]
	v_fma_mix_f32 v214, v21, s44, v214 op_sel_hi:[1,0,0]
	s_nop 0
	v_fma_mixlo_f16 v235, v86, s44, v214 op_sel_hi:[1,0,0]
	v_fma_mix_f32 v215, v86, s44, v215 op_sel:[1,0,0] op_sel_hi:[1,0,0]
	v_fma_mixhi_f16 v235, v21, s44, v215 op_sel:[1,0,0] op_sel_hi:[1,0,0]
	v_fma_mix_f32 v216, v25, s44, v216 op_sel_hi:[1,0,0]
	v_fma_mix_f32 v217, v25, s44, v217 op_sel:[1,0,0] op_sel_hi:[1,0,0]
	v_fma_mix_f32 v218, v24, s44, v218 op_sel_hi:[1,0,0]
	ds_write_b128 v16, v[232:235] offset:8704
	v_fma_mixlo_f16 v236, v96, s44, v216 op_sel_hi:[1,0,0]
	s_nop 0
	v_fma_mixhi_f16 v236, v96, s44, v217 op_sel:[1,0,0] op_sel_hi:[1,0,0]
	v_fma_mix_f32 v219, v24, s44, v219 op_sel:[1,0,0] op_sel_hi:[1,0,0]
	v_fma_mixlo_f16 v237, v84, s44, v218 op_sel_hi:[1,0,0]
	s_nop 0
	v_fma_mixhi_f16 v237, v84, s44, v219 op_sel:[1,0,0] op_sel_hi:[1,0,0]
	v_fma_mix_f32 v220, v11, s44, v220 op_sel_hi:[1,0,0]
	v_fma_mix_f32 v221, v11, s44, v221 op_sel:[1,0,0] op_sel_hi:[1,0,0]
	v_fma_mixlo_f16 v238, v23, s44, v220 op_sel_hi:[1,0,0]
	s_nop 0
	v_fma_mixhi_f16 v238, v23, s44, v221 op_sel:[1,0,0] op_sel_hi:[1,0,0]
	v_fma_mix_f32 v223, v22, s44, v223 op_sel:[1,0,0] op_sel_hi:[1,0,0]
	v_fma_mix_f32 v222, v10, s44, v222 op_sel_hi:[1,0,0]
	v_fma_mixhi_f16 v239, v10, s44, v223 op_sel:[1,0,0] op_sel_hi:[1,0,0]
	s_nop 0
	v_fma_mixlo_f16 v239, v22, s44, v222 op_sel_hi:[1,0,0]
	s_cmpk_lt_u32 s15, 0x180
	s_cselect_b64 s[8:9], -1, 0
	s_cmpk_gt_u32 s15, 0x17f
	ds_write_b128 v16, v[236:239] offset:13056
	s_cbranch_scc1 .LBB2_3
	s_load_dwordx2 s[10:11], s[0:1], 0x78
	s_load_dwordx4 s[24:27], s[0:1], 0x50
	v_mov_b32_e32 v2, v0
	s_ashr_i32 s13, s12, 31
	s_lshl_b64 s[22:23], s[12:13], 12
	s_waitcnt lgkmcnt(0)
	s_add_u32 s10, s10, s22
	v_lshlrev_b32_e32 v2, 3, v2
	s_addc_u32 s11, s11, s23
	v_and_b32_e32 v2, 0x1f8, v2
	global_load_dwordx2 v[136:137], v2, s[10:11]
	global_load_dwordx2 v[132:133], v2, s[10:11] offset:512
	global_load_dwordx2 v[128:129], v2, s[10:11] offset:1024
	global_load_dwordx2 v[124:125], v2, s[10:11] offset:1536
	global_load_dwordx2 v[134:135], v2, s[10:11] offset:2048
	global_load_dwordx2 v[130:131], v2, s[10:11] offset:2560
	global_load_dwordx2 v[126:127], v2, s[10:11] offset:3072
	global_load_dwordx2 v[122:123], v2, s[10:11] offset:3584
	s_lshl_b32 s2, s14, 4
	s_lshl_b32 s10, s19, 3
	s_add_i32 s10, s10, s2
	s_sub_i32 s2, s10, 32
	s_lshl_b64 s[2:3], s[2:3], 10
	v_lshl_or_b32 v2, v2, 1, s2
	v_mov_b32_e32 v3, s3
	v_lshl_add_u64 v[4:5], s[24:25], 0, v[2:3]
	global_load_dwordx4 v[18:21], v[4:5], off
	global_load_dwordx4 v[102:105], v[4:5], off offset:1024
	global_load_dwordx4 v[94:97], v[4:5], off offset:2048
	global_load_dwordx4 v[86:89], v[4:5], off offset:3072
	v_add_co_u32_e32 v4, vcc, s21, v4
	v_lshl_add_u64 v[6:7], s[26:27], 0, v[2:3]
	s_nop 0
	v_addc_co_u32_e32 v5, vcc, 0, v5, vcc
	global_load_dwordx4 v[78:81], v[4:5], off
	global_load_dwordx4 v[74:77], v[4:5], off offset:1024
	global_load_dwordx4 v[70:73], v[4:5], off offset:2048
	global_load_dwordx4 v[66:69], v[4:5], off offset:3072
	s_nop 0
	global_load_dwordx4 v[2:5], v[6:7], off
	global_load_dwordx4 v[118:121], v[6:7], off offset:1024
	global_load_dwordx4 v[114:117], v[6:7], off offset:2048
	global_load_dwordx4 v[110:113], v[6:7], off offset:3072
	v_add_co_u32_e32 v6, vcc, s21, v6
	s_nop 1
	v_addc_co_u32_e32 v7, vcc, 0, v7, vcc
	global_load_dwordx4 v[106:109], v[6:7], off
	global_load_dwordx4 v[98:101], v[6:7], off offset:1024
	global_load_dwordx4 v[90:93], v[6:7], off offset:2048
	global_load_dwordx4 v[82:85], v[6:7], off offset:3072
	s_branch .LBB2_4

_Z7k_layerILi0EEvPKDF16_S1_PKfS3_S3_S3_S3_S3_S1_S1_S1_S1_S3_S3_PKhS5_PDF16_S6_PfS7_:
	s_ashr_i32 s3, s2, 1
	s_and_b32 s3, s3, -8
	s_and_b32 s16, s2, 7
	v_readfirstlane_b32 s15, v0
	s_or_b32 s12, s3, s16
	s_bfe_u32 s14, s2, 0x10003
	s_cmpk_gt_u32 s15, 0xff
	s_mov_b64 s[2:3], -1
	s_cbranch_scc0 .LBB3_17
	s_mov_b32 s44, 0x3e000000
	v_mov_b32_e32 v240, 0x64646464
	s_mov_b32 s42, 0x4010400
	s_mov_b32 s43, 0x4030402
	s_load_dwordx4 s[8:11], s[0:1], 0x0
	s_load_dwordx2 s[4:5], s[0:1], 0x80
	v_add_u32_e32 v1, 0xffffff00, v0
	s_ashr_i32 s13, s12, 31
	s_lshr_b32 s17, s15, 6
	v_ashrrev_i32_e32 v2, 4, v1
	v_lshlrev_b32_e32 v3, 3, v0
	s_lshl_b64 s[2:3], s[12:13], 14
	v_and_b32_e32 v82, 0x78, v3
	v_ashrrev_i32_e32 v3, 31, v2
	s_waitcnt lgkmcnt(0)
	s_add_u32 s2, s10, s2
	s_addc_u32 s3, s11, s3
	v_lshlrev_b64 v[4:5], 8, v[2:3]
	v_lshl_add_u64 v[4:5], s[2:3], 0, v[4:5]
	v_lshlrev_b32_e32 v6, 1, v82
	v_mov_b32_e32 v7, 0
	v_lshl_add_u64 v[4:5], v[4:5], 0, v[6:7]
	s_movk_i32 s2, 0x2000
	v_add_co_u32_e32 v8, vcc, s2, v4
	global_load_dwordx4 v[74:77], v[4:5], off
	s_nop 0
	v_addc_co_u32_e32 v9, vcc, 0, v5, vcc
	global_load_dwordx4 v[78:81], v[8:9], off offset:-4096
	global_load_dwordx4 v[66:69], v[8:9], off
	s_movk_i32 s2, 0x3000
	v_add_co_u32_e32 v4, vcc, s2, v4
	s_lshl_b32 s18, s12, 9
	s_nop 0
	v_addc_co_u32_e32 v5, vcc, 0, v5, vcc
	global_load_dwordx4 v[62:65], v[4:5], off
	v_add_u32_e32 v3, s18, v2
	s_mov_b32 s7, 0x20000
	s_mov_b32 s6, 0x1000000
	v_lshl_or_b32 v3, v3, 8, v6
	s_and_b32 s9, s9, 0xffff
	s_mov_b32 s10, s6
	s_mov_b32 s11, s7
	v_add_u32_e32 v4, 0x1000, v3
	buffer_load_dwordx4 v[58:61], v3, s[8:11], 0 offen sc1
	buffer_load_dwordx4 v[50:53], v4, s[8:11], 0 offen sc1
	v_add_u32_e32 v4, 0x2000, v3
	v_add_u32_e32 v5, 0x3000, v3
	buffer_load_dwordx4 v[42:45], v4, s[8:11], 0 offen sc1
	buffer_load_dwordx4 v[34:37], v5, s[8:11], 0 offen sc1
	v_add_u32_e32 v4, 0x4000, v3
	v_add_u32_e32 v5, 0x5000, v3
	buffer_load_dwordx4 v[70:73], v4, s[8:11], 0 offen sc1
	buffer_load_dwordx4 v[54:57], v5, s[8:11], 0 offen sc1
	v_add_u32_e32 v4, 0x6000, v3
	v_add_u32_e32 v3, 0x7000, v3
	buffer_load_dwordx4 v[46:49], v4, s[8:11], 0 offen sc1
	buffer_load_dwordx4 v[38:41], v3, s[8:11], 0 offen sc1
	s_or_b32 s2, s18, 0x80
	v_add_u32_e32 v2, s2, v2
	v_lshl_or_b32 v6, v2, 8, v6
	v_add_u32_e32 v2, 0x1000, v6
	v_add_u32_e32 v7, 0x2000, v6
	v_add_u32_e32 v8, 0x3000, v6
	buffer_load_dwordx4 v[26:29], v6, s[8:11], 0 offen sc1
	buffer_load_dwordx4 v[18:21], v2, s[8:11], 0 offen sc1
	buffer_load_dwordx4 v[10:13], v7, s[8:11], 0 offen sc1
	s_nop 0
	buffer_load_dwordx4 v[2:5], v8, s[8:11], 0 offen sc1
	v_add_u32_e32 v7, 0x4000, v6
	v_add_u32_e32 v8, 0x5000, v6
	v_add_u32_e32 v83, 0x6000, v6
	buffer_load_dwordx4 v[30:33], v7, s[8:11], 0 offen sc1
	buffer_load_dwordx4 v[22:25], v8, s[8:11], 0 offen sc1
	v_add_u32_e32 v84, 0x7000, v6
	buffer_load_dwordx4 v[14:17], v83, s[8:11], 0 offen sc1
	buffer_load_dwordx4 v[6:9], v84, s[8:11], 0 offen sc1
	v_lshlrev_b32_e32 v92, 2, v82
	v_or_b32_e32 v82, 0x1e600, v92
	s_barrier
	ds_read_b128 v[82:85], v82
	v_or_b32_e32 v86, 0x1ea00, v92
	ds_read_b128 v[88:91], v86
	v_or_b32_e32 v93, 0x1e800, v92
	v_or_b32_e32 v102, 0x1ec00, v92
	s_waitcnt lgkmcnt(1)
	v_cvt_pk_f16_f32 v82, v82, v83
	v_cvt_pk_f16_f32 v83, v84, v85
	v_or_b32_e32 v84, 0x1e610, v92
	ds_read_b128 v[84:87], v84
	v_or_b32_e32 v94, 0x1ea10, v92
	v_or_b32_e32 v108, 0x1e810, v92
	v_or_b32_e32 v109, 0x1ec10, v92
	ds_read_b128 v[94:97], v94
	ds_read_b128 v[98:101], v93
	ds_read_b128 v[102:105], v102
	s_waitcnt lgkmcnt(3)
	v_cvt_pk_f16_f32 v84, v84, v85
	s_movk_i32 s22, 0x110
	s_or_b32 s21, s18, 0x100
	s_or_b32 s19, s18, 0x180
	v_mov_b32_e32 v130, v0
	s_lshl_b32 s18, s14, 6
	v_mov_b32_e32 v132, 0x11000
	s_and_b32 s5, s5, 0xffff
	s_lshl_b32 s2, s2, 7
	s_or_b32 s2, s2, s18
	s_mov_b32 s3, 0
	s_movk_i32 s20, 0x1000
	s_waitcnt vmcnt(19)
	v_cvt_f32_f16_e32 v92, v74
	v_cvt_f32_f16_sdwa v93, v74 dst_sel:DWORD dst_unused:UNUSED_PAD src0_sel:WORD_1
	s_waitcnt vmcnt(18)
	v_cvt_f32_f16_e32 v106, v78
	v_cvt_f32_f16_sdwa v107, v78 dst_sel:DWORD dst_unused:UNUSED_PAD src0_sel:WORD_1
	v_cvt_pk_f16_f32 v74, v86, v87
	s_waitcnt lgkmcnt(1)
	v_pk_fma_f32 v[86:87], v[98:99], v[92:93], v[88:89]
	v_pk_fma_f32 v[92:93], v[98:99], v[106:107], v[88:89]
	s_waitcnt lgkmcnt(0)
	v_pk_add_f32 v[92:93], v[102:103], v[92:93]
	s_waitcnt vmcnt(17)
	v_cvt_f32_f16_e32 v106, v66
	v_cvt_f32_f16_sdwa v107, v66 dst_sel:DWORD dst_unused:UNUSED_PAD src0_sel:WORD_1
	v_cvt_pk_f16_f32 v85, v92, v93
	s_waitcnt vmcnt(16)
	v_cvt_f32_f16_e32 v92, v62
	v_cvt_f32_f16_sdwa v93, v62 dst_sel:DWORD dst_unused:UNUSED_PAD src0_sel:WORD_1
	v_cvt_f32_f16_e32 v66, v67
	v_cvt_f32_f16_sdwa v67, v67 dst_sel:DWORD dst_unused:UNUSED_PAD src0_sel:WORD_1
	v_cvt_f32_f16_e32 v62, v63
	v_cvt_f32_f16_sdwa v63, v63 dst_sel:DWORD dst_unused:UNUSED_PAD src0_sel:WORD_1
	v_pk_fma_f32 v[106:107], v[98:99], v[106:107], v[88:89]
	v_pk_fma_f32 v[88:89], v[98:99], v[92:93], v[88:89]
	v_cvt_f32_f16_e32 v92, v75
	v_cvt_f32_f16_sdwa v93, v75 dst_sel:DWORD dst_unused:UNUSED_PAD src0_sel:WORD_1
	v_cvt_f32_f16_e32 v98, v79
	v_cvt_f32_f16_sdwa v99, v79 dst_sel:DWORD dst_unused:UNUSED_PAD src0_sel:WORD_1
	v_pk_add_f32 v[88:89], v[102:103], v[88:89]
	v_pk_fma_f32 v[66:67], v[100:101], v[66:67], v[90:91]
	v_pk_fma_f32 v[62:63], v[100:101], v[62:63], v[90:91]
	v_cvt_pk_f16_f32 v75, v88, v89
	v_pk_fma_f32 v[88:89], v[100:101], v[92:93], v[90:91]
	v_pk_fma_f32 v[92:93], v[100:101], v[98:99], v[90:91]
	v_pk_add_f32 v[66:67], v[104:105], v[66:67]
	v_pk_add_f32 v[62:63], v[104:105], v[62:63]
	v_pk_add_f32 v[86:87], v[102:103], v[86:87]
	v_pk_add_f32 v[106:107], v[102:103], v[106:107]
	v_pk_add_f32 v[88:89], v[104:105], v[88:89]
	v_pk_add_f32 v[92:93], v[104:105], v[92:93]
	v_cvt_pk_f16_f32 v79, v66, v67
	ds_read_b128 v[98:101], v108
	ds_read_b128 v[102:105], v109
	v_cvt_f32_f16_e32 v66, v76
	v_cvt_f32_f16_sdwa v67, v76 dst_sel:DWORD dst_unused:UNUSED_PAD src0_sel:WORD_1
	v_cvt_pk_f16_f32 v76, v62, v63
	v_cvt_f32_f16_e32 v62, v80
	v_cvt_f32_f16_sdwa v63, v80 dst_sel:DWORD dst_unused:UNUSED_PAD src0_sel:WORD_1
	s_waitcnt lgkmcnt(1)
	v_pk_fma_f32 v[66:67], v[98:99], v[66:67], v[94:95]
	v_cvt_pk_f16_f32 v87, v86, v87
	s_waitcnt lgkmcnt(0)
	v_pk_add_f32 v[66:67], v[102:103], v[66:67]
	v_pk_fma_f32 v[62:63], v[98:99], v[62:63], v[94:95]
	v_cvt_pk_f16_f32 v88, v88, v89
	v_pk_add_f32 v[62:63], v[102:103], v[62:63]
	v_cvt_pk_f16_f32 v86, v92, v93
	v_cvt_pk_f16_f32 v92, v66, v67
	v_cvt_f32_f16_e32 v66, v68
	v_cvt_f32_f16_sdwa v67, v68 dst_sel:DWORD dst_unused:UNUSED_PAD src0_sel:WORD_1
	v_cvt_pk_f16_f32 v89, v62, v63
	v_cvt_f32_f16_e32 v62, v64
	v_cvt_f32_f16_sdwa v63, v64 dst_sel:DWORD dst_unused:UNUSED_PAD src0_sel:WORD_1
	v_pk_fma_f32 v[66:67], v[98:99], v[66:67], v[94:95]
	v_cvt_pk_f16_f32 v78, v106, v107
	v_pk_add_f32 v[66:67], v[102:103], v[66:67]
	v_pk_fma_f32 v[62:63], v[98:99], v[62:63], v[94:95]
	v_cvt_pk_f16_f32 v80, v66, v67
	v_pk_add_f32 v[62:63], v[102:103], v[62:63]
	v_cvt_f32_f16_e32 v66, v77
	v_cvt_f32_f16_sdwa v67, v77 dst_sel:DWORD dst_unused:UNUSED_PAD src0_sel:WORD_1
	v_cvt_pk_f16_f32 v77, v62, v63
	v_cvt_f32_f16_e32 v62, v81
	v_cvt_f32_f16_sdwa v63, v81 dst_sel:DWORD dst_unused:UNUSED_PAD src0_sel:WORD_1
	v_pk_fma_f32 v[66:67], v[100:101], v[66:67], v[96:97]
	s_waitcnt vmcnt(15)
	v_pk_fma_f16 v59, v83, v59, v88
	v_pk_add_f32 v[66:67], v[104:105], v[66:67]
	v_pk_fma_f32 v[62:63], v[100:101], v[62:63], v[96:97]
	v_cvt_pk_f16_f32 v95, v66, v67
	v_pk_add_f32 v[62:63], v[104:105], v[62:63]
	v_cvt_f32_f16_e32 v66, v69
	v_cvt_pk_f16_f32 v93, v62, v63
	v_cvt_f32_f16_e32 v62, v65
	v_cvt_f32_f16_sdwa v63, v65 dst_sel:DWORD dst_unused:UNUSED_PAD src0_sel:WORD_1
	v_cvt_f32_f16_sdwa v67, v69 dst_sel:DWORD dst_unused:UNUSED_PAD src0_sel:WORD_1
	v_pk_fma_f16 v61, v74, v61, v95
	v_pk_fma_f16 v58, v82, v58, v87
	v_pk_fma_f32 v[62:63], v[100:101], v[62:63], v[96:97]
	v_pk_fma_f32 v[64:65], v[100:101], v[66:67], v[96:97]
	v_pk_add_f32 v[62:63], v[104:105], v[62:63]
	v_pk_add_f32 v[64:65], v[104:105], v[64:65]
	v_cvt_pk_f16_f32 v81, v62, v63
	v_mov_b32_e32 v62, v0
	v_cvt_pk_f16_f32 v91, v64, v65
	v_add_u32_e32 v63, 0xffffff00, v62
	v_lshlrev_b32_e32 v62, 4, v62
	v_ashrrev_i32_e32 v94, 4, v63
	v_and_b32_e32 v90, 0xf0, v62
	v_pk_fma_f16 v60, v84, v60, v92
	s_waitcnt vmcnt(11)
	v_pk_fma_f16 v62, v82, v70, v87
	v_pk_fma_f16 v51, v83, v51, v86
	v_pk_fma_f16 v53, v74, v53, v93
	v_pk_fma_f16 v50, v82, v50, v85
	v_pk_fma_f16 v52, v84, v52, v89
	v_pk_fma_f16 v43, v83, v43, v79
	v_pk_fma_f16 v45, v74, v45, v91
	v_pk_fma_f16 v42, v82, v42, v78
	v_pk_fma_f16 v44, v84, v44, v80
	v_pk_fma_f16 v35, v83, v35, v76
	v_pk_fma_f16 v37, v74, v37, v81
	v_pk_fma_f16 v34, v82, v34, v75
	v_pk_fma_f16 v36, v84, v36, v77
	s_waitcnt vmcnt(8)
	v_pk_fma_f16 v38, v82, v38, v75
	v_pk_fma_f16 v63, v83, v71, v88
	v_pk_fma_f16 v65, v74, v73, v95
	v_pk_fma_f16 v64, v84, v72, v92
	v_pk_max_f16 v60, v60, 0
	v_pk_max_f16 v58, v58, 0
	v_pk_max_f16 v61, v61, 0
	v_pk_max_f16 v59, v59, 0
	v_pk_max_f16 v62, v62, 0
	v_mad_u64_u32 v[96:97], s[24:25], v94, s22, v[90:91]
	v_pk_fma_f16 v55, v83, v55, v86
	v_pk_fma_f16 v57, v74, v57, v93
	v_pk_fma_f16 v54, v82, v54, v85
	v_pk_fma_f16 v56, v84, v56, v89
	v_pk_max_f16 v52, v52, 0
	v_pk_max_f16 v50, v50, 0
	v_pk_max_f16 v53, v53, 0
	v_pk_max_f16 v51, v51, 0
	v_pk_fma_f16 v47, v83, v47, v79
	v_pk_fma_f16 v49, v74, v49, v91
	v_pk_fma_f16 v46, v82, v46, v78
	v_pk_fma_f16 v48, v84, v48, v80
	v_pk_max_f16 v44, v44, 0
	v_pk_max_f16 v42, v42, 0
	v_pk_max_f16 v45, v45, 0
	v_pk_max_f16 v43, v43, 0
	v_pk_fma_f16 v39, v83, v39, v76
	v_pk_fma_f16 v41, v74, v41, v81
	v_pk_fma_f16 v40, v84, v40, v77
	v_pk_max_f16 v36, v36, 0
	v_pk_max_f16 v34, v34, 0
	v_pk_max_f16 v37, v37, 0
	v_pk_max_f16 v35, v35, 0
	v_pk_max_f16 v38, v38, 0
	v_pk_max_f16 v64, v64, 0
	v_pk_max_f16 v65, v65, 0
	v_pk_max_f16 v63, v63, 0
	ds_write_b128 v96, v[58:61]
	ds_write_b128 v96, v[62:65] offset:17408
	v_pk_add_f16 v73, v58, v62
	v_pk_max_f16 v56, v56, 0
	v_pk_max_f16 v54, v54, 0
	v_pk_max_f16 v57, v57, 0
	v_pk_max_f16 v55, v55, 0
	ds_write_b128 v96, v[50:53] offset:4352
	ds_write_b128 v96, v[54:57] offset:21760
	v_pk_max_f16 v48, v48, 0
	v_pk_max_f16 v46, v46, 0
	v_pk_max_f16 v49, v49, 0
	v_pk_max_f16 v47, v47, 0
	ds_write_b128 v96, v[42:45] offset:8704
	ds_write_b128 v96, v[46:49] offset:26112
	v_pk_max_f16 v40, v40, 0
	v_pk_max_f16 v41, v41, 0
	v_pk_max_f16 v39, v39, 0
	ds_write_b128 v96, v[34:37] offset:13056
	ds_write_b128 v96, v[38:41] offset:30464
	s_waitcnt lgkmcnt(0)
	s_barrier
	v_pk_add_f16 v62, v34, v38
	v_add_u32_e32 v34, s21, v94
	v_lshl_or_b32 v38, v34, 8, v90
	v_pk_add_f16 v71, v60, v64
	v_pk_add_f16 v60, v35, v39
	v_add_u32_e32 v34, 0x1000, v38
	v_add_u32_e32 v39, 0x2000, v38
	v_pk_add_f16 v69, v61, v65
	v_pk_add_f16 v72, v59, v63
	v_pk_add_f16 v65, v53, v57
	v_pk_add_f16 v67, v52, v56
	v_pk_add_f16 v68, v51, v55
	v_pk_add_f16 v70, v50, v54
	v_pk_add_f16 v61, v45, v49
	v_pk_add_f16 v63, v44, v48
	v_pk_add_f16 v64, v43, v47
	v_pk_add_f16 v66, v42, v46
	v_pk_add_f16 v58, v37, v41
	v_pk_add_f16 v59, v36, v40
	buffer_load_dwordx4 v[100:103], v38, s[8:11], 0 offen sc1
	buffer_load_dwordx4 v[50:53], v34, s[8:11], 0 offen sc1
	v_add_u32_e32 v40, 0x3000, v38
	buffer_load_dwordx4 v[42:45], v39, s[8:11], 0 offen sc1
	buffer_load_dwordx4 v[34:37], v40, s[8:11], 0 offen sc1
	v_add_u32_e32 v39, 0x4000, v38
	v_add_u32_e32 v40, 0x5000, v38
	buffer_load_dwordx4 v[104:107], v39, s[8:11], 0 offen sc1
	buffer_load_dwordx4 v[54:57], v40, s[8:11], 0 offen sc1
	v_add_u32_e32 v90, 0x6000, v38
	v_add_u32_e32 v94, 0x7000, v38
	buffer_load_dwordx4 v[46:49], v90, s[8:11], 0 offen sc1
	buffer_load_dwordx4 v[38:41], v94, s[8:11], 0 offen sc1
	v_mov_b32_e32 v90, v0
	s_waitcnt vmcnt(15)
	v_pk_fma_f16 v27, v83, v27, v88
	v_add_u32_e32 v94, 0xffffff00, v90
	v_lshlrev_b32_e32 v90, 4, v90
	v_ashrrev_i32_e32 v109, 4, v94
	v_and_b32_e32 v108, 0xf0, v90
	v_pk_fma_f16 v29, v74, v29, v95
	v_pk_fma_f16 v26, v82, v26, v87
	v_pk_fma_f16 v28, v84, v28, v92
	s_waitcnt vmcnt(11)
	v_pk_fma_f16 v30, v82, v30, v87
	v_pk_fma_f16 v19, v83, v19, v86
	v_pk_fma_f16 v21, v74, v21, v93
	v_pk_fma_f16 v18, v82, v18, v85
	v_pk_fma_f16 v20, v84, v20, v89
	v_pk_fma_f16 v11, v83, v11, v79
	v_pk_fma_f16 v13, v74, v13, v91
	v_pk_fma_f16 v10, v82, v10, v78
	v_pk_fma_f16 v12, v84, v12, v80
	v_pk_fma_f16 v3, v83, v3, v76
	v_pk_fma_f16 v5, v74, v5, v81
	v_pk_fma_f16 v2, v82, v2, v75
	v_pk_fma_f16 v4, v84, v4, v77
	s_waitcnt vmcnt(8)
	v_pk_fma_f16 v6, v82, v6, v75
	v_pk_fma_f16 v31, v83, v31, v88
	v_pk_fma_f16 v33, v74, v33, v95
	v_pk_fma_f16 v32, v84, v32, v92
	v_pk_max_f16 v28, v28, 0
	v_pk_max_f16 v26, v26, 0
	v_pk_max_f16 v29, v29, 0
	v_pk_max_f16 v27, v27, 0
	v_pk_max_f16 v30, v30, 0
	v_mad_u64_u32 v[110:111], s[24:25], v109, s22, v[108:109]
	v_pk_fma_f16 v23, v83, v23, v86
	v_pk_fma_f16 v25, v74, v25, v93
	v_pk_fma_f16 v22, v82, v22, v85
	v_pk_fma_f16 v24, v84, v24, v89
	v_pk_max_f16 v20, v20, 0
	v_pk_max_f16 v18, v18, 0
	v_pk_max_f16 v21, v21, 0
	v_pk_max_f16 v19, v19, 0
	v_pk_fma_f16 v15, v83, v15, v79
	v_pk_fma_f16 v17, v74, v17, v91
	v_pk_fma_f16 v14, v82, v14, v78
	v_pk_fma_f16 v16, v84, v16, v80
	v_pk_max_f16 v12, v12, 0
	v_pk_max_f16 v10, v10, 0
	v_pk_max_f16 v13, v13, 0
	v_pk_max_f16 v11, v11, 0
	v_pk_fma_f16 v7, v83, v7, v76
	v_pk_fma_f16 v9, v74, v9, v81
	v_pk_fma_f16 v8, v84, v8, v77
	v_pk_max_f16 v4, v4, 0
	v_pk_max_f16 v2, v2, 0
	v_pk_max_f16 v5, v5, 0
	v_pk_max_f16 v3, v3, 0
	v_pk_max_f16 v6, v6, 0
	v_pk_max_f16 v32, v32, 0
	v_pk_max_f16 v33, v33, 0
	v_pk_max_f16 v31, v31, 0
	ds_write_b128 v110, v[26:29] offset:34816
	ds_write_b128 v110, v[30:33] offset:52224
	v_pk_add_f16 v129, v26, v30
	v_pk_max_f16 v24, v24, 0
	v_pk_max_f16 v22, v22, 0
	v_pk_max_f16 v25, v25, 0
	v_pk_max_f16 v23, v23, 0
	ds_write_b128 v110, v[18:21] offset:39168
	ds_write_b128 v110, v[22:25] offset:56576
	v_pk_max_f16 v16, v16, 0
	v_pk_max_f16 v14, v14, 0
	v_pk_max_f16 v17, v17, 0
	v_pk_max_f16 v15, v15, 0
	ds_write_b128 v110, v[10:13] offset:43520
	ds_write_b128 v110, v[14:17] offset:60928
	v_pk_max_f16 v8, v8, 0
	v_pk_max_f16 v9, v9, 0
	v_pk_max_f16 v7, v7, 0
	ds_write_b128 v110, v[2:5] offset:47872
	ds_write_b128 v110, v[6:9] offset:65280
	v_pk_add_f16 v30, v2, v6
	v_add_u32_e32 v2, s19, v109
	v_lshl_or_b32 v6, v2, 8, v108
	v_pk_add_f16 v99, v28, v32
	v_pk_add_f16 v128, v27, v31
	v_pk_add_f16 v27, v4, v8
	v_pk_add_f16 v28, v3, v7
	v_add_u32_e32 v2, 0x1000, v6
	v_add_u32_e32 v7, 0x2000, v6
	v_add_u32_e32 v8, 0x3000, v6
	v_pk_add_f16 v97, v29, v33
	v_pk_add_f16 v33, v21, v25
	v_pk_add_f16 v94, v20, v24
	v_pk_add_f16 v96, v19, v23
	v_pk_add_f16 v98, v18, v22
	v_pk_add_f16 v29, v13, v17
	v_pk_add_f16 v31, v12, v16
	v_pk_add_f16 v32, v11, v15
	v_pk_add_f16 v90, v10, v14
	v_pk_add_f16 v26, v5, v9
	buffer_load_dwordx4 v[108:111], v6, s[8:11], 0 offen sc1
	buffer_load_dwordx4 v[18:21], v2, s[8:11], 0 offen sc1
	buffer_load_dwordx4 v[10:13], v7, s[8:11], 0 offen sc1
	s_nop 0
	buffer_load_dwordx4 v[2:5], v8, s[8:11], 0 offen sc1
	v_add_u32_e32 v7, 0x4000, v6
	v_add_u32_e32 v8, 0x5000, v6
	v_add_u32_e32 v116, 0x6000, v6
	buffer_load_dwordx4 v[112:115], v7, s[8:11], 0 offen sc1
	buffer_load_dwordx4 v[22:25], v8, s[8:11], 0 offen sc1
	v_add_u32_e32 v117, 0x7000, v6
	buffer_load_dwordx4 v[14:17], v116, s[8:11], 0 offen sc1
	buffer_load_dwordx4 v[6:9], v117, s[8:11], 0 offen sc1
	v_fma_mix_f32 v192, v73, s44, 0 op_sel_hi:[1,0,0]
	v_fma_mix_f32 v193, v73, s44, 0 op_sel:[1,0,0] op_sel_hi:[1,0,0]
	v_fma_mix_f32 v192, v129, s44, v192 op_sel_hi:[1,0,0]
	v_fma_mix_f32 v193, v129, s44, v193 op_sel:[1,0,0] op_sel_hi:[1,0,0]
	v_fma_mix_f32 v194, v72, s44, 0 op_sel_hi:[1,0,0]
	v_fma_mix_f32 v195, v72, s44, 0 op_sel:[1,0,0] op_sel_hi:[1,0,0]
	v_fma_mix_f32 v194, v128, s44, v194 op_sel_hi:[1,0,0]
	v_fma_mix_f32 v195, v128, s44, v195 op_sel:[1,0,0] op_sel_hi:[1,0,0]
	v_fma_mix_f32 v196, v71, s44, 0 op_sel_hi:[1,0,0]
	v_fma_mix_f32 v197, v71, s44, 0 op_sel:[1,0,0] op_sel_hi:[1,0,0]
	v_fma_mix_f32 v196, v99, s44, v196 op_sel_hi:[1,0,0]
	v_fma_mix_f32 v197, v99, s44, v197 op_sel:[1,0,0] op_sel_hi:[1,0,0]
	v_fma_mix_f32 v198, v69, s44, 0 op_sel_hi:[1,0,0]
	v_fma_mix_f32 v199, v69, s44, 0 op_sel:[1,0,0] op_sel_hi:[1,0,0]
	v_fma_mix_f32 v198, v97, s44, v198 op_sel_hi:[1,0,0]
	v_fma_mix_f32 v199, v97, s44, v199 op_sel:[1,0,0] op_sel_hi:[1,0,0]
	v_fma_mix_f32 v200, v70, s44, 0 op_sel_hi:[1,0,0]
	v_fma_mix_f32 v201, v70, s44, 0 op_sel:[1,0,0] op_sel_hi:[1,0,0]
	v_fma_mix_f32 v200, v98, s44, v200 op_sel_hi:[1,0,0]
	v_fma_mix_f32 v201, v98, s44, v201 op_sel:[1,0,0] op_sel_hi:[1,0,0]
	v_fma_mix_f32 v202, v68, s44, 0 op_sel_hi:[1,0,0]
	v_fma_mix_f32 v203, v68, s44, 0 op_sel:[1,0,0] op_sel_hi:[1,0,0]
	v_fma_mix_f32 v202, v96, s44, v202 op_sel_hi:[1,0,0]
	v_fma_mix_f32 v203, v96, s44, v203 op_sel:[1,0,0] op_sel_hi:[1,0,0]
	v_fma_mix_f32 v204, v67, s44, 0 op_sel_hi:[1,0,0]
	v_fma_mix_f32 v205, v67, s44, 0 op_sel:[1,0,0] op_sel_hi:[1,0,0]
	v_fma_mix_f32 v204, v94, s44, v204 op_sel_hi:[1,0,0]
	v_fma_mix_f32 v205, v94, s44, v205 op_sel:[1,0,0] op_sel_hi:[1,0,0]
	v_fma_mix_f32 v206, v65, s44, 0 op_sel_hi:[1,0,0]
	v_fma_mix_f32 v207, v65, s44, 0 op_sel:[1,0,0] op_sel_hi:[1,0,0]
	v_fma_mix_f32 v206, v33, s44, v206 op_sel_hi:[1,0,0]
	v_fma_mix_f32 v207, v33, s44, v207 op_sel:[1,0,0] op_sel_hi:[1,0,0]
	v_fma_mix_f32 v208, v66, s44, 0 op_sel_hi:[1,0,0]
	v_fma_mix_f32 v209, v66, s44, 0 op_sel:[1,0,0] op_sel_hi:[1,0,0]
	v_fma_mix_f32 v208, v90, s44, v208 op_sel_hi:[1,0,0]
	v_fma_mix_f32 v209, v90, s44, v209 op_sel:[1,0,0] op_sel_hi:[1,0,0]
	v_fma_mix_f32 v210, v64, s44, 0 op_sel_hi:[1,0,0]
	v_fma_mix_f32 v211, v64, s44, 0 op_sel:[1,0,0] op_sel_hi:[1,0,0]
	v_fma_mix_f32 v210, v32, s44, v210 op_sel_hi:[1,0,0]
	v_fma_mix_f32 v211, v32, s44, v211 op_sel:[1,0,0] op_sel_hi:[1,0,0]
	v_fma_mix_f32 v212, v63, s44, 0 op_sel_hi:[1,0,0]
	v_fma_mix_f32 v213, v63, s44, 0 op_sel:[1,0,0] op_sel_hi:[1,0,0]
	v_fma_mix_f32 v212, v31, s44, v212 op_sel_hi:[1,0,0]
	v_fma_mix_f32 v213, v31, s44, v213 op_sel:[1,0,0] op_sel_hi:[1,0,0]
	v_fma_mix_f32 v214, v61, s44, 0 op_sel_hi:[1,0,0]
	v_fma_mix_f32 v215, v61, s44, 0 op_sel:[1,0,0] op_sel_hi:[1,0,0]
	v_fma_mix_f32 v214, v29, s44, v214 op_sel_hi:[1,0,0]
	v_fma_mix_f32 v215, v29, s44, v215 op_sel:[1,0,0] op_sel_hi:[1,0,0]
	v_fma_mix_f32 v216, v62, s44, 0 op_sel_hi:[1,0,0]
	v_fma_mix_f32 v217, v62, s44, 0 op_sel:[1,0,0] op_sel_hi:[1,0,0]
	v_fma_mix_f32 v216, v30, s44, v216 op_sel_hi:[1,0,0]
	v_fma_mix_f32 v217, v30, s44, v217 op_sel:[1,0,0] op_sel_hi:[1,0,0]
	v_fma_mix_f32 v218, v60, s44, 0 op_sel_hi:[1,0,0]
	v_fma_mix_f32 v219, v60, s44, 0 op_sel:[1,0,0] op_sel_hi:[1,0,0]
	v_fma_mix_f32 v218, v28, s44, v218 op_sel_hi:[1,0,0]
	v_fma_mix_f32 v219, v28, s44, v219 op_sel:[1,0,0] op_sel_hi:[1,0,0]
	v_fma_mix_f32 v220, v59, s44, 0 op_sel_hi:[1,0,0]
	v_fma_mix_f32 v221, v59, s44, 0 op_sel:[1,0,0] op_sel_hi:[1,0,0]
	v_fma_mix_f32 v220, v27, s44, v220 op_sel_hi:[1,0,0]
	v_fma_mix_f32 v221, v27, s44, v221 op_sel:[1,0,0] op_sel_hi:[1,0,0]
	v_fma_mix_f32 v222, v58, s44, 0 op_sel_hi:[1,0,0]
	v_fma_mix_f32 v223, v58, s44, 0 op_sel:[1,0,0] op_sel_hi:[1,0,0]
	v_fma_mix_f32 v222, v26, s44, v222 op_sel_hi:[1,0,0]
	v_fma_mix_f32 v223, v26, s44, v223 op_sel:[1,0,0] op_sel_hi:[1,0,0]
	s_waitcnt lgkmcnt(0)
	s_barrier
	s_lshl_b32 s8, s12, 16
	v_add_u32_e32 v116, 0xffffff00, v130
	v_lshlrev_b32_e32 v117, 3, v130
	v_lshrrev_b32_e32 v131, 4, v116
	v_and_b32_e32 v117, 56, v117
	v_lshrrev_b32_e32 v125, 3, v116
	v_ashrrev_i32_e32 v116, 3, v116
	s_movk_i32 s10, 0xffc0
	s_or_b32 s8, s8, s18
	v_lshl_or_b32 v124, v117, 1, v132
	v_bfi_b32 v121, s10, v116, v125
	s_movk_i32 s11, 0x90
	v_or_b32_e32 v120, s8, v117
	v_mad_u64_u32 v[116:117], s[8:9], v121, s11, v[124:125]
	ds_read_b128 v[116:119], v116
	v_lshlrev_b32_e32 v133, 1, v120
	v_lshrrev_b32_e32 v127, 3, v130
	v_ashrrev_i32_e32 v120, 3, v130
	v_bfi_b32 v134, s10, v120, v127
	v_lshl_add_u32 v126, v121, 8, v133
	v_mad_u64_u32 v[120:121], s[8:9], v134, s11, v[124:125]
	ds_read_b128 v[120:123], v120
	s_waitcnt lgkmcnt(1)
	buffer_store_dwordx4 v[116:119], v126, s[4:7], 0 offen sc1
	v_lshl_add_u32 v134, v134, 8, v133
	s_waitcnt vmcnt(16)
	v_pk_fma_f16 v100, v82, v100, v87
	v_add_u32_e32 v116, 0x100, v130
	v_ashrrev_i32_e32 v116, 3, v116
	v_bfi_b32 v135, s10, v116, v125
	v_mad_u64_u32 v[116:117], s[8:9], v135, s11, v[124:125]
	v_add_u32_e32 v125, 0x200, v130
	v_ashrrev_i32_e32 v125, 3, v125
	v_bfi_b32 v136, s10, v125, v127
	ds_read_b128 v[116:119], v116
	v_mad_u64_u32 v[124:125], s[8:9], v136, s11, v[124:125]
	ds_read_b128 v[124:127], v124
	s_waitcnt lgkmcnt(2)
	buffer_store_dwordx4 v[120:123], v134, s[4:7], 0 offen sc1
	v_pk_fma_f16 v101, v83, v101, v88
	v_pk_fma_f16 v102, v84, v102, v92
	v_lshl_add_u32 v120, v135, 8, v133
	s_waitcnt lgkmcnt(1)
	buffer_store_dwordx4 v[116:119], v120, s[4:7], 0 offen sc1
	v_pk_fma_f16 v103, v74, v103, v95
	s_waitcnt vmcnt(17)
	v_pk_fma_f16 v50, v82, v50, v85
	v_lshl_add_u32 v116, v136, 8, v133
	s_waitcnt lgkmcnt(0)
	buffer_store_dwordx4 v[124:127], v116, s[4:7], 0 offen sc1
	v_lshlrev_b32_e32 v116, 4, v130
	v_and_b32_e32 v116, 0xf0, v116
	v_pk_fma_f16 v51, v83, v51, v86
	v_pk_fma_f16 v52, v84, v52, v89
	v_pk_fma_f16 v53, v74, v53, v93
	s_waitcnt vmcnt(14)
	v_pk_fma_f16 v56, v84, v56, v89
	v_pk_fma_f16 v57, v74, v57, v93
	v_pk_fma_f16 v42, v82, v42, v78
	v_pk_fma_f16 v43, v83, v43, v79
	v_pk_fma_f16 v44, v84, v44, v80
	v_pk_fma_f16 v45, v74, v45, v91
	s_waitcnt vmcnt(13)
	v_pk_fma_f16 v46, v82, v46, v78
	v_pk_fma_f16 v47, v83, v47, v79
	v_pk_fma_f16 v104, v82, v104, v87
	v_pk_fma_f16 v105, v83, v105, v88
	v_pk_fma_f16 v106, v84, v106, v92
	v_pk_fma_f16 v107, v74, v107, v95
	v_pk_max_f16 v103, v103, 0
	v_pk_max_f16 v102, v102, 0
	v_pk_max_f16 v101, v101, 0
	v_pk_max_f16 v100, v100, 0
	v_mad_u64_u32 v[116:117], s[8:9], v131, s22, v[116:117]
	v_pk_fma_f16 v54, v82, v54, v85
	v_pk_fma_f16 v55, v83, v55, v86
	v_pk_max_f16 v53, v53, 0
	v_pk_max_f16 v52, v52, 0
	v_pk_max_f16 v51, v51, 0
	v_pk_max_f16 v50, v50, 0
	v_pk_max_f16 v57, v57, 0
	v_pk_max_f16 v56, v56, 0
	v_pk_fma_f16 v48, v84, v48, v80
	v_pk_fma_f16 v49, v74, v49, v91
	v_pk_max_f16 v45, v45, 0
	v_pk_max_f16 v44, v44, 0
	v_pk_max_f16 v43, v43, 0
	v_pk_max_f16 v42, v42, 0
	v_pk_max_f16 v47, v47, 0
	v_pk_max_f16 v46, v46, 0
	v_pk_max_f16 v107, v107, 0
	v_pk_max_f16 v106, v106, 0
	v_pk_max_f16 v105, v105, 0
	v_pk_max_f16 v104, v104, 0
	ds_write_b128 v116, v[100:103]
	ds_write_b128 v116, v[104:107] offset:17408
	v_pk_max_f16 v55, v55, 0
	v_pk_max_f16 v54, v54, 0
	ds_write_b128 v116, v[50:53] offset:4352
	ds_write_b128 v116, v[54:57] offset:21760
	v_pk_add_f16 v53, v53, v57
	v_pk_add_f16 v52, v52, v56
	v_pk_max_f16 v49, v49, 0
	v_pk_max_f16 v48, v48, 0
	ds_write_b128 v116, v[42:45] offset:8704
	ds_write_b128 v116, v[46:49] offset:26112
	v_pk_add_f16 v56, v43, v47
	v_pk_add_f16 v57, v42, v46
	v_pk_fma_f16 v34, v82, v34, v75
	v_pk_fma_f16 v35, v83, v35, v76
	v_pk_fma_f16 v36, v84, v36, v77
	v_pk_fma_f16 v37, v74, v37, v81
	s_waitcnt vmcnt(12)
	v_pk_fma_f16 v42, v82, v38, v75
	v_pk_fma_f16 v43, v83, v39, v76
	v_pk_add_f16 v100, v100, v104
	v_pk_add_f16 v51, v51, v55
	v_pk_add_f16 v50, v50, v54
	v_pk_add_f16 v54, v45, v49
	v_pk_add_f16 v55, v44, v48
	v_pk_fma_f16 v44, v84, v40, v77
	v_pk_fma_f16 v45, v74, v41, v81
	v_pk_max_f16 v41, v37, 0
	v_pk_max_f16 v40, v36, 0
	v_pk_max_f16 v39, v35, 0
	v_pk_max_f16 v38, v34, 0
	v_pk_max_f16 v43, v43, 0
	v_pk_max_f16 v42, v42, 0
	v_mov_b32_e32 v104, v0
	v_pk_max_f16 v45, v45, 0
	v_pk_max_f16 v44, v44, 0
	ds_write_b128 v116, v[38:41] offset:13056
	ds_write_b128 v116, v[42:45] offset:30464
	v_pk_add_f16 v36, v39, v43
	v_pk_add_f16 v37, v38, v42
	s_waitcnt lgkmcnt(0)
	s_barrier
	v_pk_add_f16 v101, v101, v105
	v_add_u32_e32 v38, 0xffffff00, v104
	v_lshlrev_b32_e32 v39, 3, v104
	v_lshrrev_b32_e32 v105, 4, v38
	v_and_b32_e32 v39, 56, v39
	v_lshrrev_b32_e32 v47, 3, v38
	v_ashrrev_i32_e32 v38, 3, v38
	v_lshl_or_b32 v46, v39, 1, v132
	v_bfi_b32 v43, s10, v38, v47
	v_or_b32_e32 v42, s2, v39
	v_mad_u64_u32 v[38:39], s[8:9], v43, s11, v[46:47]
	v_pk_add_f16 v34, v41, v45
	v_pk_add_f16 v35, v40, v44
	ds_read_b128 v[38:41], v38 offset:18432
	v_pk_add_f16 v102, v102, v106
	v_lshlrev_b32_e32 v106, 1, v42
	v_lshrrev_b32_e32 v49, 3, v104
	v_ashrrev_i32_e32 v42, 3, v104
	v_pk_add_f16 v103, v103, v107
	v_bfi_b32 v107, s10, v42, v49
	v_lshl_add_u32 v48, v43, 8, v106
	v_mad_u64_u32 v[42:43], s[8:9], v107, s11, v[46:47]
	ds_read_b128 v[42:45], v42 offset:18432
	s_waitcnt lgkmcnt(1)
	buffer_store_dwordx4 v[38:41], v48, s[4:7], 0 offen sc1
	v_lshl_add_u32 v107, v107, 8, v106
	s_waitcnt vmcnt(11)
	v_pk_fma_f16 v18, v82, v18, v85
	v_add_u32_e32 v38, 0x100, v104
	v_ashrrev_i32_e32 v38, 3, v38
	v_bfi_b32 v116, s10, v38, v47
	v_mad_u64_u32 v[38:39], s[8:9], v116, s11, v[46:47]
	v_add_u32_e32 v47, 0x200, v104
	v_ashrrev_i32_e32 v47, 3, v47
	v_bfi_b32 v117, s10, v47, v49
	ds_read_b128 v[38:41], v38 offset:18432
	v_mad_u64_u32 v[46:47], s[8:9], v117, s11, v[46:47]
	ds_read_b128 v[46:49], v46 offset:18432
	s_waitcnt lgkmcnt(2)
	buffer_store_dwordx4 v[42:45], v107, s[4:7], 0 offen sc1
	v_pk_fma_f16 v19, v83, v19, v86
	v_pk_fma_f16 v20, v84, v20, v89
	v_lshl_add_u32 v42, v116, 8, v106
	s_waitcnt lgkmcnt(1)
	buffer_store_dwordx4 v[38:41], v42, s[4:7], 0 offen sc1
	v_pk_fma_f16 v21, v74, v21, v93
	s_waitcnt vmcnt(9)
	v_pk_fma_f16 v24, v84, v24, v89
	v_lshl_add_u32 v38, v117, 8, v106
	s_waitcnt lgkmcnt(0)
	buffer_store_dwordx4 v[46:49], v38, s[4:7], 0 offen sc1
	v_lshlrev_b32_e32 v38, 4, v104
	v_pk_fma_f16 v39, v83, v109, v88
	v_and_b32_e32 v46, 0xf0, v38
	v_pk_fma_f16 v38, v82, v108, v87
	v_pk_fma_f16 v40, v84, v110, v92
	v_pk_fma_f16 v41, v74, v111, v95
	v_pk_fma_f16 v25, v74, v25, v93
	v_pk_fma_f16 v10, v82, v10, v78
	v_pk_fma_f16 v11, v83, v11, v79
	v_pk_fma_f16 v12, v84, v12, v80
	v_pk_fma_f16 v13, v74, v13, v91
	v_pk_fma_f16 v2, v82, v2, v75
	v_pk_fma_f16 v3, v83, v3, v76
	v_pk_fma_f16 v4, v84, v4, v77
	v_pk_fma_f16 v5, v74, v5, v81
	s_waitcnt vmcnt(8)
	v_pk_fma_f16 v6, v82, v6, v75
	v_pk_fma_f16 v7, v83, v7, v76
	v_pk_fma_f16 v42, v82, v112, v87
	v_pk_fma_f16 v43, v83, v113, v88
	v_pk_fma_f16 v44, v84, v114, v92
	v_pk_fma_f16 v45, v74, v115, v95
	v_pk_max_f16 v41, v41, 0
	v_pk_max_f16 v40, v40, 0
	v_pk_max_f16 v39, v39, 0
	v_pk_max_f16 v38, v38, 0
	v_mad_u64_u32 v[46:47], s[8:9], v105, s22, v[46:47]
	v_pk_fma_f16 v22, v82, v22, v85
	v_pk_fma_f16 v23, v83, v23, v86
	v_pk_max_f16 v21, v21, 0
	v_pk_max_f16 v20, v20, 0
	v_pk_max_f16 v19, v19, 0
	v_pk_max_f16 v18, v18, 0
	v_pk_max_f16 v25, v25, 0
	v_pk_max_f16 v24, v24, 0
	v_pk_fma_f16 v14, v82, v14, v78
	v_pk_fma_f16 v15, v83, v15, v79
	v_pk_fma_f16 v16, v84, v16, v80
	v_pk_fma_f16 v17, v74, v17, v91
	v_pk_max_f16 v13, v13, 0
	v_pk_max_f16 v12, v12, 0
	v_pk_max_f16 v11, v11, 0
	v_pk_max_f16 v10, v10, 0
	v_pk_fma_f16 v8, v84, v8, v77
	v_pk_fma_f16 v9, v74, v9, v81
	v_pk_max_f16 v5, v5, 0
	v_pk_max_f16 v4, v4, 0
	v_pk_max_f16 v3, v3, 0
	v_pk_max_f16 v2, v2, 0
	v_pk_max_f16 v7, v7, 0
	v_pk_max_f16 v6, v6, 0
	v_pk_max_f16 v45, v45, 0
	v_pk_max_f16 v44, v44, 0
	v_pk_max_f16 v43, v43, 0
	v_pk_max_f16 v42, v42, 0
	ds_write_b128 v46, v[38:41] offset:34816
	ds_write_b128 v46, v[42:45] offset:52224
	v_pk_max_f16 v23, v23, 0
	v_pk_max_f16 v22, v22, 0
	ds_write_b128 v46, v[18:21] offset:39168
	ds_write_b128 v46, v[22:25] offset:56576
	v_pk_add_f16 v21, v21, v25
	v_pk_add_f16 v20, v20, v24
	v_pk_max_f16 v17, v17, 0
	v_pk_max_f16 v16, v16, 0
	v_pk_max_f16 v15, v15, 0
	v_pk_max_f16 v14, v14, 0
	ds_write_b128 v46, v[10:13] offset:43520
	ds_write_b128 v46, v[14:17] offset:60928
	v_pk_max_f16 v9, v9, 0
	v_pk_max_f16 v8, v8, 0
	ds_write_b128 v46, v[2:5] offset:47872
	ds_write_b128 v46, v[6:9] offset:65280
	v_pk_add_f16 v24, v3, v7
	v_pk_add_f16 v25, v2, v6
	v_pk_add_f16 v19, v19, v23
	v_pk_add_f16 v18, v18, v22
	v_pk_add_f16 v22, v5, v9
	v_pk_add_f16 v23, v4, v8
	v_pk_add_f16 v38, v38, v42
	v_fma_mix_f32 v192, v100, s44, v192 op_sel_hi:[1,0,0]
	v_fma_mix_f32 v193, v100, s44, v193 op_sel:[1,0,0] op_sel_hi:[1,0,0]
	v_fma_mixlo_f16 v224, v38, s44, v192 op_sel_hi:[1,0,0]
	s_nop 0
	v_fma_mixhi_f16 v224, v38, s44, v193 op_sel:[1,0,0] op_sel_hi:[1,0,0]
	v_pk_add_f16 v39, v39, v43
	v_fma_mix_f32 v194, v101, s44, v194 op_sel_hi:[1,0,0]
	v_fma_mix_f32 v195, v101, s44, v195 op_sel:[1,0,0] op_sel_hi:[1,0,0]
	v_pk_add_f16 v15, v11, v15
	v_pk_add_f16 v14, v10, v14
	v_fma_mixlo_f16 v225, v39, s44, v194 op_sel_hi:[1,0,0]
	s_nop 0
	v_fma_mixhi_f16 v225, v39, s44, v195 op_sel:[1,0,0] op_sel_hi:[1,0,0]
	s_mov_b32 s2, 0x3e000000
	v_pk_add_f16 v40, v40, v44
	v_fma_mix_f32 v196, v102, s44, v196 op_sel_hi:[1,0,0]
	v_fma_mix_f32 v197, v102, s44, v197 op_sel:[1,0,0] op_sel_hi:[1,0,0]
	v_fma_mixlo_f16 v226, v40, s44, v196 op_sel_hi:[1,0,0]
	s_nop 0
	v_fma_mixhi_f16 v226, v40, s44, v197 op_sel:[1,0,0] op_sel_hi:[1,0,0]
	v_pk_add_f16 v41, v41, v45
	v_fma_mix_f32 v198, v103, s44, v198 op_sel_hi:[1,0,0]
	v_fma_mix_f32 v199, v103, s44, v199 op_sel:[1,0,0] op_sel_hi:[1,0,0]
	v_pk_add_f16 v17, v13, v17
	v_pk_add_f16 v16, v12, v16
	v_fma_mixlo_f16 v227, v41, s44, v198 op_sel_hi:[1,0,0]
	s_nop 0
	v_fma_mixhi_f16 v227, v41, s44, v199 op_sel:[1,0,0] op_sel_hi:[1,0,0]
	v_add_u32_e32 v38, 0x1a000, v46
	v_fma_mix_f32 v200, v18, s44, v200 op_sel_hi:[1,0,0]
	v_fma_mix_f32 v201, v18, s44, v201 op_sel:[1,0,0] op_sel_hi:[1,0,0]
	ds_write_b128 v38, v[224:227]
	v_fma_mixlo_f16 v228, v50, s44, v200 op_sel_hi:[1,0,0]
	s_nop 0
	v_fma_mixhi_f16 v228, v50, s44, v201 op_sel:[1,0,0] op_sel_hi:[1,0,0]
	v_fma_mix_f32 v202, v19, s44, v202 op_sel_hi:[1,0,0]
	s_nop 0
	v_fma_mixlo_f16 v229, v51, s44, v202 op_sel_hi:[1,0,0]
	v_fma_mix_f32 v203, v51, s44, v203 op_sel:[1,0,0] op_sel_hi:[1,0,0]
	v_fma_mixhi_f16 v229, v19, s44, v203 op_sel:[1,0,0] op_sel_hi:[1,0,0]
	v_fma_mix_f32 v204, v52, s44, v204 op_sel_hi:[1,0,0]
	v_fma_mix_f32 v205, v52, s44, v205 op_sel:[1,0,0] op_sel_hi:[1,0,0]
	v_fma_mixlo_f16 v230, v20, s44, v204 op_sel_hi:[1,0,0]
	s_nop 0
	v_fma_mixhi_f16 v230, v20, s44, v205 op_sel:[1,0,0] op_sel_hi:[1,0,0]
	v_fma_mix_f32 v206, v21, s44, v206 op_sel_hi:[1,0,0]
	s_nop 0
	v_fma_mixlo_f16 v231, v53, s44, v206 op_sel_hi:[1,0,0]
	v_fma_mix_f32 v207, v53, s44, v207 op_sel:[1,0,0] op_sel_hi:[1,0,0]
	v_fma_mixhi_f16 v231, v21, s44, v207 op_sel:[1,0,0] op_sel_hi:[1,0,0]
	v_fma_mix_f32 v208, v14, s44, v208 op_sel_hi:[1,0,0]
	v_fma_mix_f32 v209, v14, s44, v209 op_sel:[1,0,0] op_sel_hi:[1,0,0]
	v_fma_mix_f32 v210, v15, s44, v210 op_sel_hi:[1,0,0]
	ds_write_b128 v38, v[228:231] offset:4352
	v_fma_mixlo_f16 v232, v57, s44, v208 op_sel_hi:[1,0,0]
	s_nop 0
	v_fma_mixhi_f16 v232, v57, s44, v209 op_sel:[1,0,0] op_sel_hi:[1,0,0]
	v_fma_mix_f32 v211, v15, s44, v211 op_sel:[1,0,0] op_sel_hi:[1,0,0]
	v_fma_mixlo_f16 v233, v56, s44, v210 op_sel_hi:[1,0,0]
	s_nop 0
	v_fma_mixhi_f16 v233, v56, s44, v211 op_sel:[1,0,0] op_sel_hi:[1,0,0]
	v_fma_mix_f32 v212, v55, s44, v212 op_sel_hi:[1,0,0]
	v_fma_mix_f32 v213, v55, s44, v213 op_sel:[1,0,0] op_sel_hi:[1,0,0]
	v_fma_mixlo_f16 v234, v16, s44, v212 op_sel_hi:[1,0,0]
	s_nop 0
	v_fma_mixhi_f16 v234, v16, s44, v213 op_sel:[1,0,0] op_sel_hi:[1,0,0]
	v_fma_mix_f32 v214, v17, s44, v214 op_sel_hi:[1,0,0]
	s_nop 0
	v_fma_mixlo_f16 v235, v54, s44, v214 op_sel_hi:[1,0,0]
	v_fma_mix_f32 v215, v54, s44, v215 op_sel:[1,0,0] op_sel_hi:[1,0,0]
	v_fma_mixhi_f16 v235, v17, s44, v215 op_sel:[1,0,0] op_sel_hi:[1,0,0]
	v_fma_mix_f32 v216, v25, s44, v216 op_sel_hi:[1,0,0]
	v_fma_mix_f32 v217, v25, s44, v217 op_sel:[1,0,0] op_sel_hi:[1,0,0]
	v_fma_mix_f32 v218, v24, s44, v218 op_sel_hi:[1,0,0]
	ds_write_b128 v38, v[232:235] offset:8704
	v_fma_mixlo_f16 v236, v37, s44, v216 op_sel_hi:[1,0,0]
	s_nop 0
	v_fma_mixhi_f16 v236, v37, s44, v217 op_sel:[1,0,0] op_sel_hi:[1,0,0]
	v_fma_mix_f32 v219, v24, s44, v219 op_sel:[1,0,0] op_sel_hi:[1,0,0]
	v_fma_mixlo_f16 v237, v36, s44, v218 op_sel_hi:[1,0,0]
	s_nop 0
	v_fma_mixhi_f16 v237, v36, s44, v219 op_sel:[1,0,0] op_sel_hi:[1,0,0]
	v_fma_mix_f32 v220, v35, s44, v220 op_sel_hi:[1,0,0]
	v_fma_mix_f32 v221, v35, s44, v221 op_sel:[1,0,0] op_sel_hi:[1,0,0]
	v_fma_mixlo_f16 v238, v23, s44, v220 op_sel_hi:[1,0,0]
	s_nop 0
	v_fma_mixhi_f16 v238, v23, s44, v221 op_sel:[1,0,0] op_sel_hi:[1,0,0]
	v_fma_mix_f32 v222, v22, s44, v222 op_sel_hi:[1,0,0]
	s_nop 0
	v_fma_mixlo_f16 v239, v34, s44, v222 op_sel_hi:[1,0,0]
	v_fma_mix_f32 v223, v34, s44, v223 op_sel:[1,0,0] op_sel_hi:[1,0,0]
	v_fma_mixhi_f16 v239, v22, s44, v223 op_sel:[1,0,0] op_sel_hi:[1,0,0]
	s_cmpk_lt_u32 s15, 0x180
	s_cselect_b64 s[8:9], -1, 0
	s_cmpk_gt_u32 s15, 0x17f
	ds_write_b128 v38, v[236:239] offset:13056
	s_cbranch_scc1 .LBB3_3
	s_load_dwordx2 s[10:11], s[0:1], 0x78
	s_load_dwordx4 s[24:27], s[0:1], 0x50
	v_mov_b32_e32 v2, v0
	s_lshl_b64 s[22:23], s[12:13], 12
	s_waitcnt lgkmcnt(0)
	s_add_u32 s10, s10, s22
	v_lshlrev_b32_e32 v2, 3, v2
	s_addc_u32 s11, s11, s23
	v_and_b32_e32 v2, 0x1f8, v2
	global_load_dwordx2 v[136:137], v2, s[10:11]
	global_load_dwordx2 v[132:133], v2, s[10:11] offset:512
	global_load_dwordx2 v[128:129], v2, s[10:11] offset:1024
	global_load_dwordx2 v[124:125], v2, s[10:11] offset:1536
	global_load_dwordx2 v[134:135], v2, s[10:11] offset:2048
	global_load_dwordx2 v[130:131], v2, s[10:11] offset:2560
	global_load_dwordx2 v[126:127], v2, s[10:11] offset:3072
	global_load_dwordx2 v[122:123], v2, s[10:11] offset:3584
	s_lshl_b32 s2, s14, 4
	s_lshl_b32 s10, s17, 3
	s_add_i32 s10, s10, s2
	s_sub_i32 s2, s10, 32
	s_lshl_b64 s[2:3], s[2:3], 10
	v_lshl_or_b32 v2, v2, 1, s2
	v_mov_b32_e32 v3, s3
	v_lshl_add_u64 v[4:5], s[24:25], 0, v[2:3]
	global_load_dwordx4 v[18:21], v[4:5], off
	global_load_dwordx4 v[102:105], v[4:5], off offset:1024
	global_load_dwordx4 v[94:97], v[4:5], off offset:2048
	global_load_dwordx4 v[86:89], v[4:5], off offset:3072
	v_add_co_u32_e32 v4, vcc, s20, v4
	v_lshl_add_u64 v[6:7], s[26:27], 0, v[2:3]
	s_nop 0
	v_addc_co_u32_e32 v5, vcc, 0, v5, vcc
	global_load_dwordx4 v[78:81], v[4:5], off
	global_load_dwordx4 v[74:77], v[4:5], off offset:1024
	global_load_dwordx4 v[70:73], v[4:5], off offset:2048
	global_load_dwordx4 v[66:69], v[4:5], off offset:3072
	s_nop 0
	global_load_dwordx4 v[2:5], v[6:7], off
	global_load_dwordx4 v[118:121], v[6:7], off offset:1024
	global_load_dwordx4 v[114:117], v[6:7], off offset:2048
	global_load_dwordx4 v[110:113], v[6:7], off offset:3072
	v_add_co_u32_e32 v6, vcc, s20, v6
	s_nop 1
	v_addc_co_u32_e32 v7, vcc, 0, v7, vcc
	global_load_dwordx4 v[106:109], v[6:7], off
	global_load_dwordx4 v[98:101], v[6:7], off offset:1024
	global_load_dwordx4 v[90:93], v[6:7], off offset:2048
	global_load_dwordx4 v[82:85], v[6:7], off offset:3072
	s_branch .LBB3_4
